# P7 second GEMM epilogue: gate_nsa loads from Z tagged nt as well
# baseline (speedup 1.0000x reference)
;     __device__ __forceinline__ void operator()(const f32x4 (&acc)[2][2][4][2], const Unit& u, int wr, int wc, int fr, int fq) const {
;     ...
;         EPB_LOAD(0);
; #pragma unroll
;         for (int kb = 0; kb < 8; ++kb) { const int ai = kb >> 2, m = kb & 3;
;             if (kb < 7) EPB_LOAD(kb + 1);
;             { const int row = row0 + ai * HALF + m * 16; float rmx = 0.f;
; #pragma unroll
;                 for (int bj = 0; bj < 2; ++bj) { const int col = col0 + bj * HALF; f32x4 v0 = acc[ai][bj][m][0], v1 = acc[ai][bj][m][1];
;                     if (QI8) { const f32x4 c0 = cb[bj][0] * ra[ai][m], c1 = cb[bj][1] * ra[ai][m]; const i32x4 i0 = __builtin_bit_cast(i32x4, v0), i1 = __builtin_bit_cast(i32x4, v1);
;                         v0 = (f32x4){(float)i0[0], (float)i0[1], (float)i0[2], (float)i0[3]} * c0; v1 = (f32x4){(float)i1[0], (float)i1[1], (float)i1[2], (float)i1[3]} * c1; }
;                     else if (MODE == 0) { v0 = v0 * tsc; v1 = v1 * tsc; }
;                     if (!QI8 && MODE == 1) { v0 = v0 * cb[bj][0]; v1 = v1 * cb[bj][1]; }
;                     if (MODE == 2 || MODE == 3) { const u32x4 g = gq[kb & 1][bj];
;                         f32x4 g0 = {sigmoidf_(bflo(g.x)), sigmoidf_(bfhi(g.x)), sigmoidf_(bflo(g.y)), sigmoidf_(bfhi(g.y))};
;                         f32x4 g1 = {sigmoidf_(bflo(g.z)), sigmoidf_(bfhi(g.z)), sigmoidf_(bflo(g.w)), sigmoidf_(bfhi(g.w))};
;                         v0 = v0 * g0; v1 = v1 * g1;
;                         if (MODE == 3) { const u32x4 q = aq[kb & 1][bj];
;                             v0 = v0 + (f32x4){bflo(q.x), bfhi(q.x), bflo(q.y), bfhi(q.y)}; v1 = v1 + (f32x4){bflo(q.z), bfhi(q.z), bflo(q.w), bfhi(q.w)}; } }
;                     if (MODE == 4) { v0 = v0 + rs[kb & 1][bj][0]; v1 = v1 + rs[kb & 1][bj][1]; }
;                     if (MODE == 5) { const u32x4 c = gq[kb & 1][bj], q = aq[kb & 1][bj];
;                         v0 = (f32x4){bflo(c.x) + sigmoidf_(v0[0]) * bflo(q.x), bfhi(c.x) + sigmoidf_(v0[1]) * bfhi(q.x), bflo(c.y) + sigmoidf_(v0[2]) * bflo(q.y), bfhi(c.y) + sigmoidf_(v0[3]) * bfhi(q.y)};
;                         v1 = (f32x4){bflo(c.z) + sigmoidf_(v1[0]) * bflo(q.z), bfhi(c.z) + sigmoidf_(v1[1]) * bfhi(q.z), bflo(c.w) + sigmoidf_(v1[2]) * bflo(q.w), bfhi(c.w) + sigmoidf_(v1[3]) * bfhi(q.w)}; }
.LBB0_1030:
	v_lshl_or_b32 v162, s34, 8, v224
	v_lshl_add_u32 v176, s36, 8, v1
	v_ashrrev_i32_e32 v163, 31, v162
	v_mov_b64_e32 v[142:143], s[14:15]
	v_ashrrev_i32_e32 v177, 31, v176
	v_mad_i64_i32 v[144:145], s[34:35], v176, s65, v[142:143]
	v_lshlrev_b64 v[166:167], 1, v[162:163]
	v_lshl_add_u64 v[138:139], v[176:177], 2, s[4:5]
	v_lshl_add_u64 v[140:141], v[162:163], 2, s[10:11]
	v_lshl_add_u64 v[144:145], v[144:145], 0, v[166:167]
	global_load_dword v182, v[138:139], off
	global_load_dwordx4 v[66:69], v[140:141], off
	global_load_dwordx4 v[62:65], v[140:141], off offset:16
	global_load_dwordx4 v[158:161], v[144:145], off nt
	v_lshlrev_b64 v[212:213], 13, v[176:177]
	v_lshl_add_u64 v[146:147], s[0:1], 0, v[212:213]
	v_lshl_add_u64 v[146:147], v[146:147], 0, v[166:167]
	global_load_dwordx4 v[186:189], v[146:147], off
	v_cvt_f32_i32_e32 v215, v57
	v_cvt_f32_i32_e32 v214, v56
	v_cvt_f32_i32_e32 v217, v55
	v_cvt_f32_i32_e32 v216, v54
	v_cvt_f32_i32_e32 v219, v53
	v_cvt_f32_i32_e32 v218, v52
	v_cvt_f32_i32_e32 v221, v51
	v_cvt_f32_i32_e32 v220, v50
	global_load_dword v184, v[138:139], off offset:64
	global_load_dword v178, v[138:139], off offset:128
	global_load_dword v174, v[138:139], off offset:192
	global_load_dword v172, v[138:139], off offset:512
	global_load_dword v170, v[138:139], off offset:576
	global_load_dword v168, v[138:139], off offset:640
	global_load_dword v164, v[138:139], off offset:704
	global_load_dwordx4 v[50:53], v[140:141], off offset:528
	global_load_dwordx4 v[54:57], v[140:141], off offset:512
	global_load_dwordx4 v[190:193], v[144:145], off offset:256 nt
	v_or_b32_e32 v180, 16, v176
	v_mad_i64_i32 v[142:143], s[34:35], v180, s65, v[142:143]
	v_lshl_add_u64 v[140:141], v[142:143], 0, v[166:167]
	global_load_dwordx4 v[154:157], v[140:141], off nt
	global_load_dwordx4 v[142:145], v[140:141], off offset:256 nt
	global_load_dwordx4 v[150:153], v[146:147], off offset:256
	v_ashrrev_i32_e32 v181, 31, v180
	v_lshlrev_b64 v[138:139], 13, v[180:181]
	v_lshl_add_u64 v[138:139], s[0:1], 0, v[138:139]
	v_lshl_add_u64 v[138:139], v[138:139], 0, v[166:167]
	global_load_dwordx4 v[146:149], v[138:139], off
	s_nop 0
	global_load_dwordx4 v[138:141], v[138:139], off offset:256
	v_cvt_f32_i32_e32 v135, v135
	v_cvt_f32_i32_e32 v134, v134
	v_cvt_f32_i32_e32 v137, v137
	v_cvt_f32_i32_e32 v136, v136
	v_cvt_f32_i32_e32 v131, v131
	v_cvt_f32_i32_e32 v130, v130
	v_cvt_f32_i32_e32 v133, v133
	v_cvt_f32_i32_e32 v132, v132
	s_waitcnt vmcnt(0)
	v_pk_mul_f32 v[222:223], v[182:183], v[68:69] op_sel_hi:[0,1]
	v_pk_mul_f32 v[230:231], v[182:183], v[66:67] op_sel_hi:[0,1]
	v_lshlrev_b32_e32 v165, 16, v158
	v_lshlrev_b32_e32 v169, 16, v159
	v_lshlrev_b32_e32 v171, 16, v160
	v_and_b32_e32 v160, 0xffff0000, v160
	v_lshlrev_b32_e32 v173, 16, v161
	v_and_b32_e32 v161, 0xffff0000, v161
	v_mul_f32_e32 v165, 0xbfb8aa3b, v165
	v_mul_f32_e32 v169, 0xbfb8aa3b, v169
	v_and_b32_e32 v159, 0xffff0000, v159
	v_mul_f32_e32 v160, 0xbfb8aa3b, v160
	v_mul_f32_e32 v175, 0xbfb8aa3b, v161
	v_exp_f32_e32 v161, v165
	v_exp_f32_e32 v165, v169
	v_and_b32_e32 v158, 0xffff0000, v158
	v_mul_f32_e32 v159, 0xbfb8aa3b, v159
	v_exp_f32_e32 v160, v160
	v_mul_f32_e32 v158, 0xbfb8aa3b, v158
	v_mul_f32_e32 v171, 0xbfb8aa3b, v171
	v_exp_f32_e32 v159, v159
	v_exp_f32_e32 v158, v158
	v_exp_f32_e32 v169, v171
	v_mul_f32_e32 v173, 0xbfb8aa3b, v173
	v_add_f32_e32 v165, 1.0, v165
	v_pk_mul_f32 v[232:233], v[182:183], v[64:65] op_sel_hi:[0,1]
	v_pk_mul_f32 v[234:235], v[182:183], v[62:63] op_sel_hi:[0,1]
	v_exp_f32_e32 v171, v173
	v_add_f32_e32 v183, 1.0, v160
	v_rcp_f32_e32 v160, v165
	v_exp_f32_e32 v165, v175
	v_add_f32_e32 v161, 1.0, v161
	v_add_f32_e32 v179, 1.0, v159
	v_add_f32_e32 v173, 1.0, v158
	v_add_f32_e32 v169, 1.0, v169
	v_rcp_f32_e32 v158, v161
	v_rcp_f32_e32 v161, v179
	v_pk_mul_f32 v[214:215], v[222:223], v[214:215]
	v_rcp_f32_e32 v159, v173
	v_rcp_f32_e32 v222, v169
	v_rcp_f32_e32 v223, v183
	v_add_f32_e32 v169, 1.0, v171
	v_add_f32_e32 v165, 1.0, v165
	v_pk_mul_f32 v[216:217], v[230:231], v[216:217]
	v_pk_mul_f32 v[218:219], v[232:233], v[218:219]
	v_rcp_f32_e32 v230, v169
	v_rcp_f32_e32 v231, v165
	v_lshlrev_b32_e32 v232, 16, v186
	v_and_b32_e32 v233, 0xffff0000, v186
	v_lshlrev_b32_e32 v186, 16, v187
	v_and_b32_e32 v187, 0xffff0000, v187
	v_pk_mul_f32 v[220:221], v[234:235], v[220:221]
	v_pk_fma_f32 v[160:161], v[214:215], v[160:161], v[186:187]
	v_lshlrev_b32_e32 v186, 16, v188
	v_and_b32_e32 v187, 0xffff0000, v188
	v_pk_fma_f32 v[158:159], v[216:217], v[158:159], v[232:233]
	v_pk_fma_f32 v[186:187], v[220:221], v[222:223], v[186:187]
	v_lshlrev_b32_e32 v188, 16, v189
	v_and_b32_e32 v189, 0xffff0000, v189
	v_cvt_pk_bf16_f32 v158, v158, v159
	v_cvt_pk_bf16_f32 v159, v160, v161
	v_cvt_pk_bf16_f32 v160, v186, v187
	v_lshl_add_u64 v[186:187], s[12:13], 0, v[212:213]
	v_pk_fma_f32 v[188:189], v[218:219], v[230:231], v[188:189]
	v_lshl_add_u64 v[186:187], v[186:187], 0, v[166:167]
	v_cvt_pk_bf16_f32 v161, v188, v189
	global_store_dwordx4 v[186:187], v[158:161], off
	v_lshlrev_b32_e32 v169, 16, v161
	v_lshlrev_b32_e32 v165, 16, v158
	v_and_b32_e32 v161, 0xffff0000, v161
	v_and_b32_e32 v158, 0xffff0000, v158
	v_max_f32_e64 v161, |v161|, |v161|
	v_max_f32_e64 v169, |v169|, |v169|
	v_max_f32_e64 v158, |v158|, |v158|
	v_max_f32_e64 v165, |v165|, |v165|
	v_max_f32_e32 v161, v169, v161
	v_lshlrev_b32_e32 v169, 16, v192
	v_max_f32_e32 v158, v165, v158
	v_lshlrev_b32_e32 v165, 16, v159
	v_and_b32_e32 v159, 0xffff0000, v159
	v_mul_f32_e32 v169, 0xbfb8aa3b, v169
	v_and_b32_e32 v171, 0xffff0000, v192
	v_max_f32_e64 v159, |v159|, |v159|
	v_max_f32_e64 v165, |v165|, |v165|
	v_exp_f32_e32 v169, v169
;     __device__ __forceinline__ void operator()(const f32x4 (&acc)[2][2][4][2], const Unit& u, int wr, int wc, int fr, int fq) const {
;     ...
;         EPB_LOAD(0);
; #pragma unroll
;         for (int kb = 0; kb < 8; ++kb) { const int ai = kb >> 2, m = kb & 3;
;             if (kb < 7) EPB_LOAD(kb + 1);
;             { const int row = row0 + ai * HALF + m * 16; float rmx = 0.f;
; #pragma unroll
;                 for (int bj = 0; bj < 2; ++bj) { const int col = col0 + bj * HALF; f32x4 v0 = acc[ai][bj][m][0], v1 = acc[ai][bj][m][1];
;                     if (QI8) { const f32x4 c0 = cb[bj][0] * ra[ai][m], c1 = cb[bj][1] * ra[ai][m]; const i32x4 i0 = __builtin_bit_cast(i32x4, v0), i1 = __builtin_bit_cast(i32x4, v1);
;                         v0 = (f32x4){(float)i0[0], (float)i0[1], (float)i0[2], (float)i0[3]} * c0; v1 = (f32x4){(float)i1[0], (float)i1[1], (float)i1[2], (float)i1[3]} * c1; }
;                     else if (MODE == 0) { v0 = v0 * tsc; v1 = v1 * tsc; }
;                     if (!QI8 && MODE == 1) { v0 = v0 * cb[bj][0]; v1 = v1 * cb[bj][1]; }
;                     if (MODE == 2 || MODE == 3) { const u32x4 g = gq[kb & 1][bj];
;                         f32x4 g0 = {sigmoidf_(bflo(g.x)), sigmoidf_(bfhi(g.x)), sigmoidf_(bflo(g.y)), sigmoidf_(bfhi(g.y))};
;                         f32x4 g1 = {sigmoidf_(bflo(g.z)), sigmoidf_(bfhi(g.z)), sigmoidf_(bflo(g.w)), sigmoidf_(bfhi(g.w))};
;                         v0 = v0 * g0; v1 = v1 * g1;
;                         if (MODE == 3) { const u32x4 q = aq[kb & 1][bj];
;                             v0 = v0 + (f32x4){bflo(q.x), bfhi(q.x), bflo(q.y), bfhi(q.y)}; v1 = v1 + (f32x4){bflo(q.z), bfhi(q.z), bflo(q.w), bfhi(q.w)}; } }
;                     if (MODE == 4) { v0 = v0 + rs[kb & 1][bj][0]; v1 = v1 + rs[kb & 1][bj][1]; }
;                     if (MODE == 5) { const u32x4 c = gq[kb & 1][bj], q = aq[kb & 1][bj];
;                         v0 = (f32x4){bflo(c.x) + sigmoidf_(v0[0]) * bflo(q.x), bfhi(c.x) + sigmoidf_(v0[1]) * bfhi(q.x), bflo(c.y) + sigmoidf_(v0[2]) * bflo(q.y), bfhi(c.y) + sigmoidf_(v0[3]) * bfhi(q.y)};
;                         v1 = (f32x4){bflo(c.z) + sigmoidf_(v1[0]) * bflo(q.z), bfhi(c.z) + sigmoidf_(v1[1]) * bfhi(q.z), bflo(c.w) + sigmoidf_(v1[2]) * bflo(q.w), bfhi(c.w) + sigmoidf_(v1[3]) * bfhi(q.w)}; }
	v_mul_f32_e32 v171, 0xbfb8aa3b, v171
	v_max_f32_e32 v159, v165, v159
	v_lshlrev_b32_e32 v165, 16, v160
	v_and_b32_e32 v160, 0xffff0000, v160
	v_exp_f32_e32 v171, v171
	v_max3_f32 v160, |v165|, |v160|, v161
	v_max3_f32 v165, v158, v159, v160
	v_pk_mul_f32 v[160:161], v[182:183], v[54:55] op_sel_hi:[0,1]
	v_pk_mul_f32 v[158:159], v[182:183], v[56:57] op_sel_hi:[0,1]
	v_pk_mul_f32 v[188:189], v[182:183], v[52:53] op_sel_hi:[0,1]
	v_pk_mul_f32 v[182:183], v[182:183], v[50:51] op_sel_hi:[0,1]
	v_pk_mul_f32 v[134:135], v[160:161], v[134:135]
	v_lshlrev_b32_e32 v160, 16, v191
	v_and_b32_e32 v161, 0xffff0000, v191
	v_add_f32_e32 v169, 1.0, v169
	v_pk_mul_f32 v[136:137], v[158:159], v[136:137]
	v_pk_mul_f32 v[130:131], v[182:183], v[130:131]
	v_lshlrev_b32_e32 v158, 16, v190
	v_and_b32_e32 v159, 0xffff0000, v190
	v_mul_f32_e32 v160, 0xbfb8aa3b, v160
	v_mul_f32_e32 v161, 0xbfb8aa3b, v161
	v_rcp_f32_e32 v182, v169
	v_add_f32_e32 v169, 1.0, v171
	v_lshlrev_b32_e32 v171, 16, v193
	v_mul_f32_e32 v158, 0xbfb8aa3b, v158
	v_mul_f32_e32 v159, 0xbfb8aa3b, v159
	v_exp_f32_e32 v160, v160
	v_exp_f32_e32 v161, v161
	v_mul_f32_e32 v171, 0xbfb8aa3b, v171
	v_and_b32_e32 v173, 0xffff0000, v193
	v_exp_f32_e32 v158, v158
	v_exp_f32_e32 v159, v159
	v_exp_f32_e32 v171, v171
	v_mul_f32_e32 v173, 0xbfb8aa3b, v173
	v_exp_f32_e32 v173, v173
	v_add_f32_e32 v160, 1.0, v160
	v_add_f32_e32 v161, 1.0, v161
	v_add_f32_e32 v158, 1.0, v158
	v_add_f32_e32 v159, 1.0, v159
	v_rcp_f32_e32 v160, v160
	v_rcp_f32_e32 v161, v161
	v_rcp_f32_e32 v183, v169
	v_add_f32_e32 v169, 1.0, v171
	v_pk_mul_f32 v[132:133], v[188:189], v[132:133]
	v_rcp_f32_e32 v158, v158
	v_rcp_f32_e32 v159, v159
	v_rcp_f32_e32 v188, v169
	v_add_f32_e32 v169, 1.0, v173
	v_rcp_f32_e32 v189, v169
	v_lshlrev_b32_e32 v190, 16, v150
	v_and_b32_e32 v191, 0xffff0000, v150
	v_lshlrev_b32_e32 v150, 16, v151
	v_and_b32_e32 v151, 0xffff0000, v151
	v_pk_fma_f32 v[136:137], v[136:137], v[160:161], v[150:151]
	v_lshlrev_b32_e32 v150, 16, v152
	v_and_b32_e32 v151, 0xffff0000, v152
	v_pk_fma_f32 v[134:135], v[134:135], v[158:159], v[190:191]
	v_lshlrev_b32_e32 v152, 16, v153
	v_and_b32_e32 v153, 0xffff0000, v153
	v_pk_fma_f32 v[130:131], v[130:131], v[182:183], v[150:151]
	v_pk_fma_f32 v[152:153], v[132:133], v[188:189], v[152:153]
	v_cvt_pk_bf16_f32 v132, v134, v135
	v_cvt_pk_bf16_f32 v133, v136, v137
	v_cvt_pk_bf16_f32 v134, v130, v131
	s_nop 0
	v_lshlrev_b32_e32 v130, 16, v132
	v_and_b32_e32 v131, 0xffff0000, v132
	v_max_f32_e64 v131, |v131|, |v131|
	v_max_f32_e64 v130, |v130|, |v130|
	v_cvt_pk_bf16_f32 v135, v152, v153
	v_max_f32_e32 v130, v130, v131
	v_lshlrev_b32_e32 v131, 16, v133
	v_and_b32_e32 v136, 0xffff0000, v133
	v_lshlrev_b32_e32 v150, 16, v135
	v_and_b32_e32 v151, 0xffff0000, v135
	v_max_f32_e64 v136, |v136|, |v136|
	v_max_f32_e64 v131, |v131|, |v131|
	v_max_f32_e64 v151, |v151|, |v151|
	v_max_f32_e64 v150, |v150|, |v150|
	v_max_f32_e32 v131, v131, v136
	v_lshlrev_b32_e32 v136, 16, v134
	v_and_b32_e32 v137, 0xffff0000, v134
	v_max_f32_e32 v150, v150, v151
	v_max3_f32 v136, |v136|, |v137|, v150
	v_max3_f32 v130, v130, v131, v136
	v_and_b32_e32 v136, 64, v228
	v_xor_b32_e32 v131, 16, v228
	v_add_u32_e32 v136, 64, v136
	v_cmp_lt_i32_e32 vcc, v131, v136
	v_max3_f32 v130, v165, 0, v130
	global_store_dwordx4 v[186:187], v[132:135], off offset:256
	v_cndmask_b32_e32 v131, v228, v131, vcc
	v_lshlrev_b32_e32 v165, 2, v131
	ds_bpermute_b32 v131, v165, v130
	s_waitcnt lgkmcnt(0)
	v_max_f32_e32 v131, v131, v131
	v_max_f32_e32 v130, v130, v131
	v_xor_b32_e32 v131, 32, v228
	v_cmp_lt_i32_e32 vcc, v131, v136
	s_nop 1
	v_cndmask_b32_e32 v131, v228, v131, vcc
	v_lshlrev_b32_e32 v169, 2, v131
	ds_bpermute_b32 v131, v169, v130
	s_and_saveexec_b64 s[34:35], s[6:7]
	s_cbranch_execz .LBB0_1032
	s_waitcnt lgkmcnt(0)
	v_max_f32_e32 v131, v131, v131
	v_max_f32_e32 v130, v130, v130
	v_lshl_add_u64 v[132:133], v[176:177], 2, s[16:17]
	v_max_f32_e32 v130, v130, v131
	global_atomic_umax v[132:133], v130, off
.LBB0_1032:
	s_or_b64 exec, exec, s[34:35]
	v_or_b32_e32 v182, 32, v176
	v_ashrrev_i32_e32 v183, 31, v182
	s_waitcnt lgkmcnt(0)
	v_mov_b64_e32 v[130:131], s[14:15]
	v_lshlrev_b64 v[132:133], 13, v[182:183]
	v_mad_i64_i32 v[130:131], s[34:35], v182, s65, v[130:131]
	v_lshl_add_u64 v[132:133], s[0:1], 0, v[132:133]
	v_lshl_add_u64 v[130:131], v[130:131], 0, v[166:167]
	v_lshl_add_u64 v[132:133], v[132:133], 0, v[166:167]
	global_load_dwordx4 v[158:161], v[130:131], off nt
	global_load_dwordx4 v[134:137], v[130:131], off offset:256 nt
	global_load_dwordx4 v[150:153], v[132:133], off
	s_nop 0
	global_load_dwordx4 v[130:133], v[132:133], off offset:256
	v_lshlrev_b32_e32 v171, 16, v154
	v_and_b32_e32 v154, 0xffff0000, v154
	v_mul_f32_e32 v171, 0xbfb8aa3b, v171
	v_mul_f32_e32 v154, 0xbfb8aa3b, v154
	v_exp_f32_e32 v171, v171
	v_exp_f32_e32 v173, v154
	v_cvt_f32_i32_e32 v129, v129
	v_cvt_f32_i32_e32 v128, v128
	v_add_f32_e32 v154, 1.0, v171
	v_add_f32_e32 v171, 1.0, v173
	v_lshlrev_b32_e32 v173, 16, v155
	v_mul_f32_e32 v173, 0xbfb8aa3b, v173
	v_exp_f32_e32 v173, v173
	v_and_b32_e32 v155, 0xffff0000, v155
	v_mul_f32_e32 v155, 0xbfb8aa3b, v155
	v_exp_f32_e32 v175, v155
	v_rcp_f32_e32 v155, v171
	v_add_f32_e32 v171, 1.0, v173
	v_lshlrev_b32_e32 v173, 16, v156
	v_mul_f32_e32 v173, 0xbfb8aa3b, v173
	v_exp_f32_e32 v173, v173
	v_and_b32_e32 v156, 0xffff0000, v156
	v_pk_mul_f32 v[188:189], v[184:185], v[68:69] op_sel_hi:[0,1]
	v_mul_f32_e32 v156, 0xbfb8aa3b, v156
	v_pk_mul_f32 v[128:129], v[188:189], v[128:129]
	v_rcp_f32_e32 v188, v171
	v_add_f32_e32 v171, 1.0, v175
	v_exp_f32_e32 v175, v156
	v_add_f32_e32 v156, 1.0, v173
	v_lshlrev_b32_e32 v173, 16, v157
;     __device__ __forceinline__ void operator()(const f32x4 (&acc)[2][2][4][2], const Unit& u, int wr, int wc, int fr, int fq) const {
;     ...
;             { const int row = row0 + ai * HALF + m * 16; float rmx = 0.f;
; #pragma unroll
;                 for (int bj = 0; bj < 2; ++bj) { const int col = col0 + bj * HALF; f32x4 v0 = acc[ai][bj][m][0], v1 = acc[ai][bj][m][1];
;                     if (QI8) { const f32x4 c0 = cb[bj][0] * ra[ai][m], c1 = cb[bj][1] * ra[ai][m]; const i32x4 i0 = __builtin_bit_cast(i32x4, v0), i1 = __builtin_bit_cast(i32x4, v1);
;                         v0 = (f32x4){(float)i0[0], (float)i0[1], (float)i0[2], (float)i0[3]} * c0; v1 = (f32x4){(float)i1[0], (float)i1[1], (float)i1[2], (float)i1[3]} * c1; }
;                     else if (MODE == 0) { v0 = v0 * tsc; v1 = v1 * tsc; }
;                     if (!QI8 && MODE == 1) { v0 = v0 * cb[bj][0]; v1 = v1 * cb[bj][1]; }
;                     if (MODE == 2 || MODE == 3) { const u32x4 g = gq[kb & 1][bj];
;                         f32x4 g0 = {sigmoidf_(bflo(g.x)), sigmoidf_(bfhi(g.x)), sigmoidf_(bflo(g.y)), sigmoidf_(bfhi(g.y))};
;                         f32x4 g1 = {sigmoidf_(bflo(g.z)), sigmoidf_(bfhi(g.z)), sigmoidf_(bflo(g.w)), sigmoidf_(bfhi(g.w))};
;                         v0 = v0 * g0; v1 = v1 * g1;
;                         if (MODE == 3) { const u32x4 q = aq[kb & 1][bj];
;                             v0 = v0 + (f32x4){bflo(q.x), bfhi(q.x), bflo(q.y), bfhi(q.y)}; v1 = v1 + (f32x4){bflo(q.z), bfhi(q.z), bflo(q.w), bfhi(q.w)}; } }
;                     if (MODE == 4) { v0 = v0 + rs[kb & 1][bj][0]; v1 = v1 + rs[kb & 1][bj][1]; }
;                     if (MODE == 5) { const u32x4 c = gq[kb & 1][bj], q = aq[kb & 1][bj];
;                         v0 = (f32x4){bflo(c.x) + sigmoidf_(v0[0]) * bflo(q.x), bfhi(c.x) + sigmoidf_(v0[1]) * bfhi(q.x), bflo(c.y) + sigmoidf_(v0[2]) * bflo(q.y), bfhi(c.y) + sigmoidf_(v0[3]) * bfhi(q.y)};
;                         v1 = (f32x4){bflo(c.z) + sigmoidf_(v1[0]) * bflo(q.z), bfhi(c.z) + sigmoidf_(v1[1]) * bfhi(q.z), bflo(c.w) + sigmoidf_(v1[2]) * bflo(q.w), bfhi(c.w) + sigmoidf_(v1[3]) * bfhi(q.w)}; }
;                     u32x4 w; w.x = cvtpk(v0[0], v0[1]); w.y = cvtpk(v0[2], v0[3]); w.z = cvtpk(v1[0], v1[1]); w.w = cvtpk(v1[2], v1[3]);
;                     *(u32x4*)(O + (size_t)row * ldo + col) = w;
	v_mul_f32_e32 v173, 0xbfb8aa3b, v173
	v_and_b32_e32 v157, 0xffff0000, v157
	v_exp_f32_e32 v173, v173
	v_mul_f32_e32 v157, 0xbfb8aa3b, v157
	v_cvt_f32_i32_e32 v127, v127
	v_cvt_f32_i32_e32 v126, v126
	v_rcp_f32_e32 v189, v171
	v_add_f32_e32 v171, 1.0, v175
	v_exp_f32_e32 v175, v157
	v_pk_mul_f32 v[190:191], v[184:185], v[66:67] op_sel_hi:[0,1]
	v_cvt_f32_i32_e32 v125, v125
	v_cvt_f32_i32_e32 v124, v124
	v_rcp_f32_e32 v157, v171
	v_add_f32_e32 v171, 1.0, v173
	v_pk_mul_f32 v[126:127], v[190:191], v[126:127]
	v_cvt_f32_i32_e32 v123, v123
	v_cvt_f32_i32_e32 v122, v122
	v_rcp_f32_e32 v154, v154
	v_rcp_f32_e32 v190, v171
	v_add_f32_e32 v171, 1.0, v175
	v_rcp_f32_e32 v156, v156
	v_rcp_f32_e32 v191, v171
	v_pk_mul_f32 v[192:193], v[184:185], v[64:65] op_sel_hi:[0,1]
	v_pk_mul_f32 v[212:213], v[184:185], v[62:63] op_sel_hi:[0,1]
	v_pk_mul_f32 v[124:125], v[192:193], v[124:125]
	v_lshlrev_b32_e32 v192, 16, v146
	v_and_b32_e32 v193, 0xffff0000, v146
	v_lshlrev_b32_e32 v146, 16, v147
	v_and_b32_e32 v147, 0xffff0000, v147
	v_lshlrev_b64 v[186:187], 12, v[180:181]
	v_pk_mul_f32 v[122:123], v[212:213], v[122:123]
	v_pk_fma_f32 v[128:129], v[128:129], v[188:189], v[146:147]
	v_pk_fma_f32 v[126:127], v[126:127], v[154:155], v[192:193]
	v_lshlrev_b32_e32 v146, 16, v148
	v_and_b32_e32 v147, 0xffff0000, v148
	v_lshlrev_b32_e32 v148, 16, v149
	v_and_b32_e32 v149, 0xffff0000, v149
	v_pk_fma_f32 v[148:149], v[124:125], v[190:191], v[148:149]
	v_pk_fma_f32 v[124:125], v[122:123], v[156:157], v[146:147]
	v_cvt_pk_bf16_f32 v122, v126, v127
	v_lshl_add_u64 v[126:127], v[186:187], 1, s[12:13]
	v_lshl_add_u64 v[126:127], v[126:127], 0, v[166:167]
	v_cvt_pk_bf16_f32 v123, v128, v129
	v_cvt_pk_bf16_f32 v124, v124, v125
	v_cvt_pk_bf16_f32 v125, v148, v149
	global_store_dwordx4 v[126:127], v[122:125], off
	v_lshlrev_b32_e32 v128, 16, v122
	v_max_f32_e64 v128, |v128|, |v128|
	v_and_b32_e32 v122, 0xffff0000, v122
	v_max_f32_e64 v122, |v122|, |v122|
	v_max_f32_e32 v122, v128, v122
	v_lshlrev_b32_e32 v128, 16, v123
	v_and_b32_e32 v123, 0xffff0000, v123
	v_lshlrev_b32_e32 v129, 16, v125
	v_and_b32_e32 v125, 0xffff0000, v125
	v_max_f32_e64 v123, |v123|, |v123|
	v_max_f32_e64 v128, |v128|, |v128|
	v_max_f32_e64 v125, |v125|, |v125|
	v_max_f32_e64 v129, |v129|, |v129|
	v_cvt_f32_i32_e32 v121, v121
	v_cvt_f32_i32_e32 v120, v120
	v_max_f32_e32 v123, v128, v123
	v_lshlrev_b32_e32 v128, 16, v124
	v_and_b32_e32 v124, 0xffff0000, v124
	v_max_f32_e32 v125, v129, v125
	v_cvt_f32_i32_e32 v119, v119
	v_cvt_f32_i32_e32 v118, v118
	v_cvt_f32_i32_e32 v117, v117
	v_cvt_f32_i32_e32 v116, v116
	v_max3_f32 v124, |v128|, |v124|, v125
	v_max3_f32 v148, v122, v123, v124
	v_pk_mul_f32 v[122:123], v[184:185], v[56:57] op_sel_hi:[0,1]
	v_pk_mul_f32 v[124:125], v[184:185], v[54:55] op_sel_hi:[0,1]
	v_pk_mul_f32 v[128:129], v[184:185], v[52:53] op_sel_hi:[0,1]
	v_pk_mul_f32 v[120:121], v[122:123], v[120:121]
	v_lshlrev_b32_e32 v122, 16, v142
	v_and_b32_e32 v123, 0xffff0000, v142
	v_pk_mul_f32 v[118:119], v[124:125], v[118:119]
	v_mul_f32_e32 v122, 0xbfb8aa3b, v122
	v_mul_f32_e32 v123, 0xbfb8aa3b, v123
	v_pk_mul_f32 v[116:117], v[128:129], v[116:117]
	v_lshlrev_b32_e32 v124, 16, v143
	v_and_b32_e32 v125, 0xffff0000, v143
	v_lshlrev_b32_e32 v128, 16, v144
	v_and_b32_e32 v129, 0xffff0000, v144
	v_exp_f32_e32 v122, v122
	v_exp_f32_e32 v123, v123
	v_mul_f32_e32 v124, 0xbfb8aa3b, v124
	v_mul_f32_e32 v125, 0xbfb8aa3b, v125
	v_mul_f32_e32 v128, 0xbfb8aa3b, v128
	v_mul_f32_e32 v129, 0xbfb8aa3b, v129
	v_lshlrev_b32_e32 v142, 16, v145
	v_and_b32_e32 v143, 0xffff0000, v145
	v_exp_f32_e32 v124, v124
	v_exp_f32_e32 v125, v125
	v_exp_f32_e32 v128, v128
	v_exp_f32_e32 v129, v129
	v_mul_f32_e32 v142, 0xbfb8aa3b, v142
	v_mul_f32_e32 v143, 0xbfb8aa3b, v143
	v_exp_f32_e32 v142, v142
	v_exp_f32_e32 v143, v143
	v_add_f32_e32 v122, 1.0, v122
	v_add_f32_e32 v123, 1.0, v123
	v_cvt_f32_i32_e32 v115, v115
	v_cvt_f32_i32_e32 v114, v114
	v_rcp_f32_e32 v122, v122
	v_rcp_f32_e32 v123, v123
	v_add_f32_e32 v124, 1.0, v124
	v_add_f32_e32 v125, 1.0, v125
	v_add_f32_e32 v128, 1.0, v128
	v_add_f32_e32 v129, 1.0, v129
	v_rcp_f32_e32 v124, v124
	v_rcp_f32_e32 v125, v125
	v_rcp_f32_e32 v128, v128
	v_rcp_f32_e32 v129, v129
	v_add_f32_e32 v142, 1.0, v142
	v_add_f32_e32 v143, 1.0, v143
	v_rcp_f32_e32 v142, v142
	v_rcp_f32_e32 v143, v143
	v_pk_mul_f32 v[146:147], v[184:185], v[50:51] op_sel_hi:[0,1]
	v_lshlrev_b32_e32 v144, 16, v138
	v_and_b32_e32 v145, 0xffff0000, v138
	v_pk_mul_f32 v[114:115], v[146:147], v[114:115]
	v_lshlrev_b32_e32 v138, 16, v139
	v_and_b32_e32 v139, 0xffff0000, v139
	v_pk_fma_f32 v[118:119], v[118:119], v[122:123], v[144:145]
	v_lshlrev_b32_e32 v122, 16, v140
	v_and_b32_e32 v123, 0xffff0000, v140
	v_pk_fma_f32 v[120:121], v[120:121], v[124:125], v[138:139]
	v_lshlrev_b32_e32 v124, 16, v141
	v_and_b32_e32 v125, 0xffff0000, v141
	v_pk_fma_f32 v[114:115], v[114:115], v[128:129], v[122:123]
	v_pk_fma_f32 v[124:125], v[116:117], v[142:143], v[124:125]
	v_cvt_pk_bf16_f32 v116, v118, v119
	v_cvt_pk_bf16_f32 v117, v120, v121
	v_cvt_pk_bf16_f32 v118, v114, v115
	s_nop 0
	v_lshlrev_b32_e32 v114, 16, v116
	v_and_b32_e32 v115, 0xffff0000, v116
	v_max_f32_e64 v115, |v115|, |v115|
	v_max_f32_e64 v114, |v114|, |v114|
	v_cvt_pk_bf16_f32 v119, v124, v125
	v_max_f32_e32 v114, v114, v115
	v_lshlrev_b32_e32 v115, 16, v117
	v_and_b32_e32 v120, 0xffff0000, v117
	v_lshlrev_b32_e32 v122, 16, v119
	v_and_b32_e32 v123, 0xffff0000, v119
	v_max_f32_e64 v120, |v120|, |v120|
	v_max_f32_e64 v115, |v115|, |v115|
	v_max_f32_e64 v123, |v123|, |v123|
	v_max_f32_e64 v122, |v122|, |v122|
	v_max_f32_e32 v115, v115, v120
	v_lshlrev_b32_e32 v120, 16, v118
	v_and_b32_e32 v121, 0xffff0000, v118
	v_max_f32_e32 v122, v122, v123
	v_max3_f32 v120, |v120|, |v121|, v122
	v_max3_f32 v114, v114, v115, v120
	v_max3_f32 v114, v148, 0, v114
	ds_bpermute_b32 v115, v165, v114
	global_store_dwordx4 v[126:127], v[116:119], off offset:256
	s_waitcnt lgkmcnt(0)
	v_max_f32_e32 v115, v115, v115
	v_max_f32_e32 v114, v114, v115
	ds_bpermute_b32 v115, v169, v114
	s_and_saveexec_b64 s[34:35], s[6:7]
	s_cbranch_execz .LBB0_1034
	s_waitcnt lgkmcnt(0)
	v_max_f32_e32 v115, v115, v115
	v_max_f32_e32 v114, v114, v114
	v_lshl_add_u64 v[116:117], v[180:181], 2, s[16:17]
	v_max_f32_e32 v114, v114, v115
	global_atomic_umax v[116:117], v114, off
;     __device__ __forceinline__ void operator()(const f32x4 (&acc)[2][2][4][2], const Unit& u, int wr, int wc, int fr, int fq) const {
;     ...
;         EPB_LOAD(0);
; #pragma unroll
;         for (int kb = 0; kb < 8; ++kb) { const int ai = kb >> 2, m = kb & 3;
;             if (kb < 7) EPB_LOAD(kb + 1);
;             { const int row = row0 + ai * HALF + m * 16; float rmx = 0.f;
; #pragma unroll
;                 for (int bj = 0; bj < 2; ++bj) { const int col = col0 + bj * HALF; f32x4 v0 = acc[ai][bj][m][0], v1 = acc[ai][bj][m][1];
;                     if (QI8) { const f32x4 c0 = cb[bj][0] * ra[ai][m], c1 = cb[bj][1] * ra[ai][m]; const i32x4 i0 = __builtin_bit_cast(i32x4, v0), i1 = __builtin_bit_cast(i32x4, v1);
;                         v0 = (f32x4){(float)i0[0], (float)i0[1], (float)i0[2], (float)i0[3]} * c0; v1 = (f32x4){(float)i1[0], (float)i1[1], (float)i1[2], (float)i1[3]} * c1; }
;                     else if (MODE == 0) { v0 = v0 * tsc; v1 = v1 * tsc; }
;                     if (!QI8 && MODE == 1) { v0 = v0 * cb[bj][0]; v1 = v1 * cb[bj][1]; }
;                     if (MODE == 2 || MODE == 3) { const u32x4 g = gq[kb & 1][bj];
;                         f32x4 g0 = {sigmoidf_(bflo(g.x)), sigmoidf_(bfhi(g.x)), sigmoidf_(bflo(g.y)), sigmoidf_(bfhi(g.y))};
;                         f32x4 g1 = {sigmoidf_(bflo(g.z)), sigmoidf_(bfhi(g.z)), sigmoidf_(bflo(g.w)), sigmoidf_(bfhi(g.w))};
;                         v0 = v0 * g0; v1 = v1 * g1;
;                         if (MODE == 3) { const u32x4 q = aq[kb & 1][bj];
;                             v0 = v0 + (f32x4){bflo(q.x), bfhi(q.x), bflo(q.y), bfhi(q.y)}; v1 = v1 + (f32x4){bflo(q.z), bfhi(q.z), bflo(q.w), bfhi(q.w)}; } }
;                     if (MODE == 4) { v0 = v0 + rs[kb & 1][bj][0]; v1 = v1 + rs[kb & 1][bj][1]; }
;                     if (MODE == 5) { const u32x4 c = gq[kb & 1][bj], q = aq[kb & 1][bj];
;                         v0 = (f32x4){bflo(c.x) + sigmoidf_(v0[0]) * bflo(q.x), bfhi(c.x) + sigmoidf_(v0[1]) * bfhi(q.x), bflo(c.y) + sigmoidf_(v0[2]) * bflo(q.y), bfhi(c.y) + sigmoidf_(v0[3]) * bfhi(q.y)};
;                         v1 = (f32x4){bflo(c.z) + sigmoidf_(v1[0]) * bflo(q.z), bfhi(c.z) + sigmoidf_(v1[1]) * bfhi(q.z), bflo(c.w) + sigmoidf_(v1[2]) * bflo(q.w), bfhi(c.w) + sigmoidf_(v1[3]) * bfhi(q.w)}; }
.LBB0_1034:
	s_or_b64 exec, exec, s[34:35]
	v_or_b32_e32 v138, 48, v176
	v_ashrrev_i32_e32 v139, 31, v138
	s_waitcnt lgkmcnt(0)
	v_mov_b64_e32 v[114:115], s[14:15]
	v_lshlrev_b64 v[116:117], 13, v[138:139]
	v_mad_i64_i32 v[114:115], s[34:35], v138, s65, v[114:115]
	v_lshl_add_u64 v[116:117], s[0:1], 0, v[116:117]
	v_lshl_add_u64 v[114:115], v[114:115], 0, v[166:167]
	v_lshl_add_u64 v[116:117], v[116:117], 0, v[166:167]
	global_load_dwordx4 v[126:129], v[114:115], off nt
	global_load_dwordx4 v[118:121], v[114:115], off offset:256 nt
	global_load_dwordx4 v[122:125], v[116:117], off
	s_nop 0
	global_load_dwordx4 v[114:117], v[116:117], off offset:256
	v_cvt_f32_i32_e32 v111, v111
	v_cvt_f32_i32_e32 v110, v110
	v_cvt_f32_i32_e32 v113, v113
	v_cvt_f32_i32_e32 v112, v112
	v_cvt_f32_i32_e32 v107, v107
	v_cvt_f32_i32_e32 v106, v106
	v_cvt_f32_i32_e32 v109, v109
	v_cvt_f32_i32_e32 v108, v108
	v_pk_mul_f32 v[142:143], v[178:179], v[68:69] op_sel_hi:[0,1]
	v_pk_mul_f32 v[144:145], v[178:179], v[66:67] op_sel_hi:[0,1]
	v_pk_mul_f32 v[146:147], v[178:179], v[64:65] op_sel_hi:[0,1]
	v_pk_mul_f32 v[148:149], v[178:179], v[62:63] op_sel_hi:[0,1]
	v_pk_mul_f32 v[110:111], v[144:145], v[110:111]
	v_pk_mul_f32 v[112:113], v[142:143], v[112:113]
	s_waitcnt vmcnt(9)
	v_lshlrev_b32_e32 v142, 16, v158
	v_and_b32_e32 v143, 0xffff0000, v158
	v_lshlrev_b32_e32 v144, 16, v159
	v_and_b32_e32 v145, 0xffff0000, v159
	v_pk_mul_f32 v[106:107], v[148:149], v[106:107]
	v_mul_f32_e32 v142, 0xbfb8aa3b, v142
	v_mul_f32_e32 v143, 0xbfb8aa3b, v143
	v_pk_mul_f32 v[108:109], v[146:147], v[108:109]
	v_mul_f32_e32 v144, 0xbfb8aa3b, v144
	v_mul_f32_e32 v145, 0xbfb8aa3b, v145
	v_lshlrev_b32_e32 v146, 16, v160
	v_and_b32_e32 v147, 0xffff0000, v160
	v_lshlrev_b32_e32 v148, 16, v161
	v_and_b32_e32 v149, 0xffff0000, v161
	v_exp_f32_e32 v142, v142
	v_exp_f32_e32 v143, v143
	v_exp_f32_e32 v144, v144
	v_exp_f32_e32 v145, v145
	v_mul_f32_e32 v146, 0xbfb8aa3b, v146
	v_mul_f32_e32 v147, 0xbfb8aa3b, v147
	v_mul_f32_e32 v148, 0xbfb8aa3b, v148
	v_mul_f32_e32 v149, 0xbfb8aa3b, v149
	v_exp_f32_e32 v146, v146
	v_exp_f32_e32 v147, v147
	v_exp_f32_e32 v148, v148
	v_exp_f32_e32 v149, v149
	v_add_f32_e32 v142, 1.0, v142
	v_add_f32_e32 v143, 1.0, v143
	v_add_f32_e32 v144, 1.0, v144
	v_add_f32_e32 v145, 1.0, v145
	v_rcp_f32_e32 v142, v142
	v_rcp_f32_e32 v143, v143
	v_rcp_f32_e32 v144, v144
	v_rcp_f32_e32 v145, v145
	v_add_f32_e32 v146, 1.0, v146
	v_add_f32_e32 v147, 1.0, v147
	v_add_f32_e32 v148, 1.0, v148
	v_add_f32_e32 v149, 1.0, v149
	v_rcp_f32_e32 v146, v146
	v_rcp_f32_e32 v147, v147
	v_rcp_f32_e32 v148, v148
	v_rcp_f32_e32 v149, v149
	s_waitcnt vmcnt(7)
	v_lshlrev_b32_e32 v154, 16, v150
	v_and_b32_e32 v155, 0xffff0000, v150
	v_lshlrev_b32_e32 v150, 16, v151
	v_and_b32_e32 v151, 0xffff0000, v151
	v_lshlrev_b64 v[140:141], 12, v[182:183]
	v_pk_fma_f32 v[112:113], v[112:113], v[144:145], v[150:151]
	v_pk_fma_f32 v[110:111], v[110:111], v[142:143], v[154:155]
	v_lshlrev_b32_e32 v142, 16, v152
	v_and_b32_e32 v143, 0xffff0000, v152
	v_lshlrev_b32_e32 v144, 16, v153
	v_and_b32_e32 v145, 0xffff0000, v153
	v_pk_fma_f32 v[144:145], v[108:109], v[148:149], v[144:145]
	v_pk_fma_f32 v[108:109], v[106:107], v[146:147], v[142:143]
	v_cvt_pk_bf16_f32 v106, v110, v111
	v_lshl_add_u64 v[110:111], v[140:141], 1, s[12:13]
	v_lshl_add_u64 v[110:111], v[110:111], 0, v[166:167]
	v_cvt_pk_bf16_f32 v107, v112, v113
	v_cvt_pk_bf16_f32 v108, v108, v109
	v_cvt_pk_bf16_f32 v109, v144, v145
	global_store_dwordx4 v[110:111], v[106:109], off
	v_lshlrev_b32_e32 v112, 16, v106
	v_max_f32_e64 v112, |v112|, |v112|
	v_and_b32_e32 v106, 0xffff0000, v106
	v_max_f32_e64 v106, |v106|, |v106|
	v_max_f32_e32 v106, v112, v106
	v_lshlrev_b32_e32 v112, 16, v107
	v_and_b32_e32 v107, 0xffff0000, v107
	v_lshlrev_b32_e32 v113, 16, v109
	v_and_b32_e32 v109, 0xffff0000, v109
	v_max_f32_e64 v107, |v107|, |v107|
	v_max_f32_e64 v112, |v112|, |v112|
	v_max_f32_e64 v109, |v109|, |v109|
	v_max_f32_e64 v113, |v113|, |v113|
	v_cvt_f32_i32_e32 v105, v105
	v_cvt_f32_i32_e32 v104, v104
	v_max_f32_e32 v107, v112, v107
	v_lshlrev_b32_e32 v112, 16, v108
	v_and_b32_e32 v108, 0xffff0000, v108
	v_max_f32_e32 v109, v113, v109
	v_cvt_f32_i32_e32 v103, v103
	v_cvt_f32_i32_e32 v102, v102
	v_cvt_f32_i32_e32 v101, v101
	v_cvt_f32_i32_e32 v100, v100
	v_max3_f32 v108, |v112|, |v108|, v109
	v_max3_f32 v142, v106, v107, v108
	v_pk_mul_f32 v[106:107], v[178:179], v[56:57] op_sel_hi:[0,1]
	v_pk_mul_f32 v[108:109], v[178:179], v[54:55] op_sel_hi:[0,1]
	v_pk_mul_f32 v[112:113], v[178:179], v[52:53] op_sel_hi:[0,1]
	v_pk_mul_f32 v[104:105], v[106:107], v[104:105]
	v_lshlrev_b32_e32 v106, 16, v134
	v_and_b32_e32 v107, 0xffff0000, v134
	v_pk_mul_f32 v[102:103], v[108:109], v[102:103]
	v_mul_f32_e32 v106, 0xbfb8aa3b, v106
	v_mul_f32_e32 v107, 0xbfb8aa3b, v107
	v_pk_mul_f32 v[100:101], v[112:113], v[100:101]
	v_lshlrev_b32_e32 v108, 16, v135
	v_and_b32_e32 v109, 0xffff0000, v135
	v_lshlrev_b32_e32 v112, 16, v136
	v_and_b32_e32 v113, 0xffff0000, v136
	v_exp_f32_e32 v106, v106
	v_exp_f32_e32 v107, v107
	v_mul_f32_e32 v108, 0xbfb8aa3b, v108
	v_mul_f32_e32 v109, 0xbfb8aa3b, v109
	v_mul_f32_e32 v112, 0xbfb8aa3b, v112
	v_mul_f32_e32 v113, 0xbfb8aa3b, v113
	v_lshlrev_b32_e32 v134, 16, v137
	v_and_b32_e32 v135, 0xffff0000, v137
	v_exp_f32_e32 v108, v108
	v_exp_f32_e32 v109, v109
	v_exp_f32_e32 v112, v112
	v_exp_f32_e32 v113, v113
	v_mul_f32_e32 v134, 0xbfb8aa3b, v134
	v_mul_f32_e32 v135, 0xbfb8aa3b, v135
	v_exp_f32_e32 v134, v134
	v_exp_f32_e32 v135, v135
	v_add_f32_e32 v106, 1.0, v106
	v_add_f32_e32 v107, 1.0, v107
	v_cvt_f32_i32_e32 v99, v99
	v_cvt_f32_i32_e32 v98, v98
	v_rcp_f32_e32 v106, v106
	v_rcp_f32_e32 v107, v107
	v_add_f32_e32 v108, 1.0, v108
	v_add_f32_e32 v109, 1.0, v109
	v_add_f32_e32 v112, 1.0, v112
	v_add_f32_e32 v113, 1.0, v113
	v_rcp_f32_e32 v108, v108
	v_rcp_f32_e32 v109, v109
	v_rcp_f32_e32 v112, v112
	v_rcp_f32_e32 v113, v113
	v_add_f32_e32 v134, 1.0, v134
	v_add_f32_e32 v135, 1.0, v135
	v_rcp_f32_e32 v134, v134
	v_rcp_f32_e32 v135, v135
	v_pk_mul_f32 v[140:141], v[178:179], v[50:51] op_sel_hi:[0,1]
	s_waitcnt vmcnt(7)
;     __device__ __forceinline__ void operator()(const f32x4 (&acc)[2][2][4][2], const Unit& u, int wr, int wc, int fr, int fq) const {
;     ...
;         EPB_LOAD(0);
; #pragma unroll
;         for (int kb = 0; kb < 8; ++kb) { const int ai = kb >> 2, m = kb & 3;
;             if (kb < 7) EPB_LOAD(kb + 1);
;             { const int row = row0 + ai * HALF + m * 16; float rmx = 0.f;
; #pragma unroll
;                 for (int bj = 0; bj < 2; ++bj) { const int col = col0 + bj * HALF; f32x4 v0 = acc[ai][bj][m][0], v1 = acc[ai][bj][m][1];
;                     if (QI8) { const f32x4 c0 = cb[bj][0] * ra[ai][m], c1 = cb[bj][1] * ra[ai][m]; const i32x4 i0 = __builtin_bit_cast(i32x4, v0), i1 = __builtin_bit_cast(i32x4, v1);
;                         v0 = (f32x4){(float)i0[0], (float)i0[1], (float)i0[2], (float)i0[3]} * c0; v1 = (f32x4){(float)i1[0], (float)i1[1], (float)i1[2], (float)i1[3]} * c1; }
;                     else if (MODE == 0) { v0 = v0 * tsc; v1 = v1 * tsc; }
;                     if (!QI8 && MODE == 1) { v0 = v0 * cb[bj][0]; v1 = v1 * cb[bj][1]; }
;                     if (MODE == 2 || MODE == 3) { const u32x4 g = gq[kb & 1][bj];
;                         f32x4 g0 = {sigmoidf_(bflo(g.x)), sigmoidf_(bfhi(g.x)), sigmoidf_(bflo(g.y)), sigmoidf_(bfhi(g.y))};
;                         f32x4 g1 = {sigmoidf_(bflo(g.z)), sigmoidf_(bfhi(g.z)), sigmoidf_(bflo(g.w)), sigmoidf_(bfhi(g.w))};
;                         v0 = v0 * g0; v1 = v1 * g1;
;                         if (MODE == 3) { const u32x4 q = aq[kb & 1][bj];
;                             v0 = v0 + (f32x4){bflo(q.x), bfhi(q.x), bflo(q.y), bfhi(q.y)}; v1 = v1 + (f32x4){bflo(q.z), bfhi(q.z), bflo(q.w), bfhi(q.w)}; } }
;                     if (MODE == 4) { v0 = v0 + rs[kb & 1][bj][0]; v1 = v1 + rs[kb & 1][bj][1]; }
;                     if (MODE == 5) { const u32x4 c = gq[kb & 1][bj], q = aq[kb & 1][bj];
;                         v0 = (f32x4){bflo(c.x) + sigmoidf_(v0[0]) * bflo(q.x), bfhi(c.x) + sigmoidf_(v0[1]) * bfhi(q.x), bflo(c.y) + sigmoidf_(v0[2]) * bflo(q.y), bfhi(c.y) + sigmoidf_(v0[3]) * bfhi(q.y)};
;                         v1 = (f32x4){bflo(c.z) + sigmoidf_(v1[0]) * bflo(q.z), bfhi(c.z) + sigmoidf_(v1[1]) * bfhi(q.z), bflo(c.w) + sigmoidf_(v1[2]) * bflo(q.w), bfhi(c.w) + sigmoidf_(v1[3]) * bfhi(q.w)}; }
	v_lshlrev_b32_e32 v136, 16, v130
	v_and_b32_e32 v137, 0xffff0000, v130
	v_pk_mul_f32 v[98:99], v[140:141], v[98:99]
	v_lshlrev_b32_e32 v130, 16, v131
	v_and_b32_e32 v131, 0xffff0000, v131
	v_pk_fma_f32 v[102:103], v[102:103], v[106:107], v[136:137]
	v_lshlrev_b32_e32 v106, 16, v132
	v_and_b32_e32 v107, 0xffff0000, v132
	v_pk_fma_f32 v[104:105], v[104:105], v[108:109], v[130:131]
	v_lshlrev_b32_e32 v108, 16, v133
	v_and_b32_e32 v109, 0xffff0000, v133
	v_pk_fma_f32 v[98:99], v[98:99], v[112:113], v[106:107]
	v_pk_fma_f32 v[108:109], v[100:101], v[134:135], v[108:109]
	v_cvt_pk_bf16_f32 v100, v102, v103
	v_cvt_pk_bf16_f32 v101, v104, v105
	v_cvt_pk_bf16_f32 v102, v98, v99
	s_nop 0
	v_lshlrev_b32_e32 v98, 16, v100
	v_and_b32_e32 v99, 0xffff0000, v100
	v_max_f32_e64 v99, |v99|, |v99|
	v_max_f32_e64 v98, |v98|, |v98|
	v_cvt_pk_bf16_f32 v103, v108, v109
	v_max_f32_e32 v98, v98, v99
	v_lshlrev_b32_e32 v99, 16, v101
	v_and_b32_e32 v104, 0xffff0000, v101
	v_lshlrev_b32_e32 v106, 16, v103
	v_and_b32_e32 v107, 0xffff0000, v103
	v_max_f32_e64 v104, |v104|, |v104|
	v_max_f32_e64 v99, |v99|, |v99|
	v_max_f32_e64 v107, |v107|, |v107|
	v_max_f32_e64 v106, |v106|, |v106|
	v_max_f32_e32 v99, v99, v104
	v_lshlrev_b32_e32 v104, 16, v102
	v_and_b32_e32 v105, 0xffff0000, v102
	v_max_f32_e32 v106, v106, v107
	v_max3_f32 v104, |v104|, |v105|, v106
	v_max3_f32 v98, v98, v99, v104
	v_max3_f32 v98, v142, 0, v98
	ds_bpermute_b32 v99, v165, v98
	global_store_dwordx4 v[110:111], v[100:103], off offset:256
	s_waitcnt lgkmcnt(0)
	v_max_f32_e32 v99, v99, v99
	v_max_f32_e32 v98, v98, v99
	ds_bpermute_b32 v99, v169, v98
	s_and_saveexec_b64 s[34:35], s[6:7]
	s_cbranch_execz .LBB0_1036
	s_waitcnt lgkmcnt(0)
	v_max_f32_e32 v99, v99, v99
	v_max_f32_e32 v98, v98, v98
	v_lshl_add_u64 v[100:101], v[182:183], 2, s[16:17]
	v_max_f32_e32 v98, v98, v99
	global_atomic_umax v[100:101], v98, off
.LBB0_1036:
	s_or_b64 exec, exec, s[34:35]
	v_add_u32_e32 v130, 0x80, v176
	v_ashrrev_i32_e32 v131, 31, v130
	s_waitcnt lgkmcnt(0)
	v_mov_b64_e32 v[98:99], s[14:15]
	v_lshlrev_b64 v[100:101], 13, v[130:131]
	v_mad_i64_i32 v[98:99], s[34:35], v130, s65, v[98:99]
	v_lshl_add_u64 v[100:101], s[0:1], 0, v[100:101]
	v_lshl_add_u64 v[98:99], v[98:99], 0, v[166:167]
	v_lshl_add_u64 v[100:101], v[100:101], 0, v[166:167]
	global_load_dwordx4 v[110:113], v[98:99], off nt
	global_load_dwordx4 v[102:105], v[98:99], off offset:256 nt
	global_load_dwordx4 v[106:109], v[100:101], off
	s_nop 0
	global_load_dwordx4 v[98:101], v[100:101], off offset:256
	v_cvt_f32_i32_e32 v97, v97
	v_cvt_f32_i32_e32 v96, v96
	v_pk_mul_f32 v[134:135], v[174:175], v[68:69] op_sel_hi:[0,1]
	v_cvt_f32_i32_e32 v95, v95
	v_cvt_f32_i32_e32 v94, v94
	v_pk_mul_f32 v[96:97], v[134:135], v[96:97]
	s_waitcnt vmcnt(9)
	v_lshlrev_b32_e32 v134, 16, v126
	v_and_b32_e32 v126, 0xffff0000, v126
	v_mul_f32_e32 v134, 0xbfb8aa3b, v134
	v_mul_f32_e32 v126, 0xbfb8aa3b, v126
	v_exp_f32_e32 v134, v134
	v_exp_f32_e32 v135, v126
	v_pk_mul_f32 v[136:137], v[174:175], v[66:67] op_sel_hi:[0,1]
	v_pk_mul_f32 v[94:95], v[136:137], v[94:95]
	v_add_f32_e32 v126, 1.0, v134
	v_add_f32_e32 v134, 1.0, v135
	v_lshlrev_b32_e32 v135, 16, v127
	v_and_b32_e32 v127, 0xffff0000, v127
	v_mul_f32_e32 v135, 0xbfb8aa3b, v135
	v_mul_f32_e32 v127, 0xbfb8aa3b, v127
	v_exp_f32_e32 v135, v135
	v_exp_f32_e32 v136, v127
	v_rcp_f32_e32 v127, v134
	v_cvt_f32_i32_e32 v93, v93
	v_add_f32_e32 v134, 1.0, v135
	v_add_f32_e32 v135, 1.0, v136
	v_lshlrev_b32_e32 v136, 16, v128
	v_and_b32_e32 v128, 0xffff0000, v128
	v_mul_f32_e32 v136, 0xbfb8aa3b, v136
	v_mul_f32_e32 v128, 0xbfb8aa3b, v128
	v_exp_f32_e32 v136, v136
	v_exp_f32_e32 v137, v128
	v_cvt_f32_i32_e32 v92, v92
	v_pk_mul_f32 v[140:141], v[174:175], v[64:65] op_sel_hi:[0,1]
	v_add_f32_e32 v128, 1.0, v136
	v_add_f32_e32 v136, 1.0, v137
	v_lshlrev_b32_e32 v137, 16, v129
	v_and_b32_e32 v129, 0xffff0000, v129
	v_mul_f32_e32 v137, 0xbfb8aa3b, v137
	v_mul_f32_e32 v129, 0xbfb8aa3b, v129
	v_pk_mul_f32 v[92:93], v[140:141], v[92:93]
	v_exp_f32_e32 v137, v137
	v_exp_f32_e32 v140, v129
	v_cvt_f32_i32_e32 v91, v91
	v_cvt_f32_i32_e32 v90, v90
	v_rcp_f32_e32 v126, v126
	v_rcp_f32_e32 v134, v134
	v_rcp_f32_e32 v135, v135
	v_rcp_f32_e32 v129, v136
	v_add_f32_e32 v136, 1.0, v137
	v_add_f32_e32 v137, 1.0, v140
	v_rcp_f32_e32 v128, v128
	v_rcp_f32_e32 v136, v136
	v_rcp_f32_e32 v137, v137
	v_pk_mul_f32 v[142:143], v[174:175], v[62:63] op_sel_hi:[0,1]
	s_waitcnt vmcnt(7)
;     __device__ __forceinline__ void operator()(const f32x4 (&acc)[2][2][4][2], const Unit& u, int wr, int wc, int fr, int fq) const {
;     ...
;             { const int row = row0 + ai * HALF + m * 16; float rmx = 0.f;
; #pragma unroll
;                 for (int bj = 0; bj < 2; ++bj) { const int col = col0 + bj * HALF; f32x4 v0 = acc[ai][bj][m][0], v1 = acc[ai][bj][m][1];
;                     if (QI8) { const f32x4 c0 = cb[bj][0] * ra[ai][m], c1 = cb[bj][1] * ra[ai][m]; const i32x4 i0 = __builtin_bit_cast(i32x4, v0), i1 = __builtin_bit_cast(i32x4, v1);
;                         v0 = (f32x4){(float)i0[0], (float)i0[1], (float)i0[2], (float)i0[3]} * c0; v1 = (f32x4){(float)i1[0], (float)i1[1], (float)i1[2], (float)i1[3]} * c1; }
;                     else if (MODE == 0) { v0 = v0 * tsc; v1 = v1 * tsc; }
;                     if (!QI8 && MODE == 1) { v0 = v0 * cb[bj][0]; v1 = v1 * cb[bj][1]; }
;                     if (MODE == 2 || MODE == 3) { const u32x4 g = gq[kb & 1][bj];
;                         f32x4 g0 = {sigmoidf_(bflo(g.x)), sigmoidf_(bfhi(g.x)), sigmoidf_(bflo(g.y)), sigmoidf_(bfhi(g.y))};
;                         f32x4 g1 = {sigmoidf_(bflo(g.z)), sigmoidf_(bfhi(g.z)), sigmoidf_(bflo(g.w)), sigmoidf_(bfhi(g.w))};
;                         v0 = v0 * g0; v1 = v1 * g1;
;                         if (MODE == 3) { const u32x4 q = aq[kb & 1][bj];
;                             v0 = v0 + (f32x4){bflo(q.x), bfhi(q.x), bflo(q.y), bfhi(q.y)}; v1 = v1 + (f32x4){bflo(q.z), bfhi(q.z), bflo(q.w), bfhi(q.w)}; } }
;                     if (MODE == 4) { v0 = v0 + rs[kb & 1][bj][0]; v1 = v1 + rs[kb & 1][bj][1]; }
;                     if (MODE == 5) { const u32x4 c = gq[kb & 1][bj], q = aq[kb & 1][bj];
;                         v0 = (f32x4){bflo(c.x) + sigmoidf_(v0[0]) * bflo(q.x), bfhi(c.x) + sigmoidf_(v0[1]) * bfhi(q.x), bflo(c.y) + sigmoidf_(v0[2]) * bflo(q.y), bfhi(c.y) + sigmoidf_(v0[3]) * bfhi(q.y)};
;                         v1 = (f32x4){bflo(c.z) + sigmoidf_(v1[0]) * bflo(q.z), bfhi(c.z) + sigmoidf_(v1[1]) * bfhi(q.z), bflo(c.w) + sigmoidf_(v1[2]) * bflo(q.w), bfhi(c.w) + sigmoidf_(v1[3]) * bfhi(q.w)}; }
;                     u32x4 w; w.x = cvtpk(v0[0], v0[1]); w.y = cvtpk(v0[2], v0[3]); w.z = cvtpk(v1[0], v1[1]); w.w = cvtpk(v1[2], v1[3]);
;                     *(u32x4*)(O + (size_t)row * ldo + col) = w;
	v_lshlrev_b32_e32 v140, 16, v122
	v_and_b32_e32 v141, 0xffff0000, v122
	v_lshlrev_b32_e32 v122, 16, v123
	v_and_b32_e32 v123, 0xffff0000, v123
	v_lshlrev_b64 v[132:133], 12, v[138:139]
	v_pk_mul_f32 v[90:91], v[142:143], v[90:91]
	v_pk_fma_f32 v[96:97], v[96:97], v[134:135], v[122:123]
	v_pk_fma_f32 v[94:95], v[94:95], v[126:127], v[140:141]
	v_lshlrev_b32_e32 v122, 16, v124
	v_and_b32_e32 v123, 0xffff0000, v124
	v_lshlrev_b32_e32 v124, 16, v125
	v_and_b32_e32 v125, 0xffff0000, v125
	v_pk_fma_f32 v[124:125], v[92:93], v[136:137], v[124:125]
	v_pk_fma_f32 v[92:93], v[90:91], v[128:129], v[122:123]
	v_cvt_pk_bf16_f32 v90, v94, v95
	v_lshl_add_u64 v[94:95], v[132:133], 1, s[12:13]
	v_lshl_add_u64 v[94:95], v[94:95], 0, v[166:167]
	v_cvt_pk_bf16_f32 v91, v96, v97
	v_cvt_pk_bf16_f32 v92, v92, v93
	v_cvt_pk_bf16_f32 v93, v124, v125
	global_store_dwordx4 v[94:95], v[90:93], off
	v_lshlrev_b32_e32 v96, 16, v90
	v_max_f32_e64 v96, |v96|, |v96|
	v_and_b32_e32 v90, 0xffff0000, v90
	v_max_f32_e64 v90, |v90|, |v90|
	v_max_f32_e32 v90, v96, v90
	v_lshlrev_b32_e32 v96, 16, v91
	v_and_b32_e32 v91, 0xffff0000, v91
	v_lshlrev_b32_e32 v97, 16, v93
	v_and_b32_e32 v93, 0xffff0000, v93
	v_max_f32_e64 v91, |v91|, |v91|
	v_max_f32_e64 v96, |v96|, |v96|
	v_max_f32_e64 v93, |v93|, |v93|
	v_max_f32_e64 v97, |v97|, |v97|
	v_cvt_f32_i32_e32 v89, v89
	v_cvt_f32_i32_e32 v88, v88
	v_max_f32_e32 v91, v96, v91
	v_lshlrev_b32_e32 v96, 16, v92
	v_and_b32_e32 v92, 0xffff0000, v92
	v_max_f32_e32 v93, v97, v93
	v_cvt_f32_i32_e32 v87, v87
	v_cvt_f32_i32_e32 v86, v86
	v_cvt_f32_i32_e32 v85, v85
	v_cvt_f32_i32_e32 v84, v84
	v_max3_f32 v92, |v96|, |v92|, v93
	v_max3_f32 v124, v90, v91, v92
	v_pk_mul_f32 v[90:91], v[174:175], v[56:57] op_sel_hi:[0,1]
	v_pk_mul_f32 v[92:93], v[174:175], v[54:55] op_sel_hi:[0,1]
	v_pk_mul_f32 v[96:97], v[174:175], v[52:53] op_sel_hi:[0,1]
	v_pk_mul_f32 v[88:89], v[90:91], v[88:89]
	v_lshlrev_b32_e32 v90, 16, v118
	v_and_b32_e32 v91, 0xffff0000, v118
	v_pk_mul_f32 v[86:87], v[92:93], v[86:87]
	v_mul_f32_e32 v90, 0xbfb8aa3b, v90
	v_mul_f32_e32 v91, 0xbfb8aa3b, v91
	v_pk_mul_f32 v[84:85], v[96:97], v[84:85]
	v_lshlrev_b32_e32 v92, 16, v119
	v_and_b32_e32 v93, 0xffff0000, v119
	v_lshlrev_b32_e32 v96, 16, v120
	v_and_b32_e32 v97, 0xffff0000, v120
	v_exp_f32_e32 v90, v90
	v_exp_f32_e32 v91, v91
	v_mul_f32_e32 v92, 0xbfb8aa3b, v92
	v_mul_f32_e32 v93, 0xbfb8aa3b, v93
	v_mul_f32_e32 v96, 0xbfb8aa3b, v96
	v_mul_f32_e32 v97, 0xbfb8aa3b, v97
	v_lshlrev_b32_e32 v118, 16, v121
	v_and_b32_e32 v119, 0xffff0000, v121
	v_exp_f32_e32 v92, v92
	v_exp_f32_e32 v93, v93
	v_exp_f32_e32 v96, v96
	v_exp_f32_e32 v97, v97
	v_mul_f32_e32 v118, 0xbfb8aa3b, v118
	v_mul_f32_e32 v119, 0xbfb8aa3b, v119
	v_exp_f32_e32 v118, v118
	v_exp_f32_e32 v119, v119
	v_add_f32_e32 v90, 1.0, v90
	v_add_f32_e32 v91, 1.0, v91
	v_cvt_f32_i32_e32 v83, v83
	v_cvt_f32_i32_e32 v82, v82
	v_rcp_f32_e32 v90, v90
	v_rcp_f32_e32 v91, v91
	v_add_f32_e32 v92, 1.0, v92
	v_add_f32_e32 v93, 1.0, v93
	v_add_f32_e32 v96, 1.0, v96
	v_add_f32_e32 v97, 1.0, v97
	v_rcp_f32_e32 v92, v92
	v_rcp_f32_e32 v93, v93
	v_rcp_f32_e32 v96, v96
	v_rcp_f32_e32 v97, v97
	v_add_f32_e32 v118, 1.0, v118
	v_add_f32_e32 v119, 1.0, v119
	v_rcp_f32_e32 v118, v118
	v_rcp_f32_e32 v119, v119
	v_pk_mul_f32 v[122:123], v[174:175], v[50:51] op_sel_hi:[0,1]
	s_waitcnt vmcnt(7)
	v_lshlrev_b32_e32 v120, 16, v114
	v_and_b32_e32 v121, 0xffff0000, v114
	v_pk_mul_f32 v[82:83], v[122:123], v[82:83]
	v_lshlrev_b32_e32 v114, 16, v115
	v_and_b32_e32 v115, 0xffff0000, v115
	v_pk_fma_f32 v[86:87], v[86:87], v[90:91], v[120:121]
	v_lshlrev_b32_e32 v90, 16, v116
	v_and_b32_e32 v91, 0xffff0000, v116
	v_pk_fma_f32 v[88:89], v[88:89], v[92:93], v[114:115]
	v_lshlrev_b32_e32 v92, 16, v117
	v_and_b32_e32 v93, 0xffff0000, v117
	v_pk_fma_f32 v[82:83], v[82:83], v[96:97], v[90:91]
	v_pk_fma_f32 v[92:93], v[84:85], v[118:119], v[92:93]
	v_cvt_pk_bf16_f32 v84, v86, v87
	v_cvt_pk_bf16_f32 v85, v88, v89
	v_cvt_pk_bf16_f32 v86, v82, v83
	s_nop 0
	v_lshlrev_b32_e32 v82, 16, v84
	v_and_b32_e32 v83, 0xffff0000, v84
	v_max_f32_e64 v83, |v83|, |v83|
	v_max_f32_e64 v82, |v82|, |v82|
	v_cvt_pk_bf16_f32 v87, v92, v93
	v_max_f32_e32 v82, v82, v83
	v_lshlrev_b32_e32 v83, 16, v85
	v_and_b32_e32 v88, 0xffff0000, v85
	v_lshlrev_b32_e32 v90, 16, v87
	v_and_b32_e32 v91, 0xffff0000, v87
	v_max_f32_e64 v88, |v88|, |v88|
	v_max_f32_e64 v83, |v83|, |v83|
	v_max_f32_e64 v91, |v91|, |v91|
	v_max_f32_e64 v90, |v90|, |v90|
	v_max_f32_e32 v83, v83, v88
	v_lshlrev_b32_e32 v88, 16, v86
	v_and_b32_e32 v89, 0xffff0000, v86
	v_max_f32_e32 v90, v90, v91
	v_max3_f32 v88, |v88|, |v89|, v90
	v_max3_f32 v82, v82, v83, v88
	v_max3_f32 v82, v124, 0, v82
	ds_bpermute_b32 v83, v165, v82
	global_store_dwordx4 v[94:95], v[84:87], off offset:256
	s_waitcnt lgkmcnt(0)
	v_max_f32_e32 v83, v83, v83
	v_max_f32_e32 v82, v82, v83
	ds_bpermute_b32 v83, v169, v82
	s_and_saveexec_b64 s[34:35], s[6:7]
	s_cbranch_execz .LBB0_1038
	s_waitcnt lgkmcnt(0)
	v_max_f32_e32 v83, v83, v83
	v_max_f32_e32 v82, v82, v82
	v_lshl_add_u64 v[84:85], v[138:139], 2, s[16:17]
	v_max_f32_e32 v82, v82, v83
	global_atomic_umax v[84:85], v82, off
;     __device__ __forceinline__ void operator()(const f32x4 (&acc)[2][2][4][2], const Unit& u, int wr, int wc, int fr, int fq) const {
;     ...
;         EPB_LOAD(0);
; #pragma unroll
;         for (int kb = 0; kb < 8; ++kb) { const int ai = kb >> 2, m = kb & 3;
;             if (kb < 7) EPB_LOAD(kb + 1);
;             { const int row = row0 + ai * HALF + m * 16; float rmx = 0.f;
; #pragma unroll
;                 for (int bj = 0; bj < 2; ++bj) { const int col = col0 + bj * HALF; f32x4 v0 = acc[ai][bj][m][0], v1 = acc[ai][bj][m][1];
;                     if (QI8) { const f32x4 c0 = cb[bj][0] * ra[ai][m], c1 = cb[bj][1] * ra[ai][m]; const i32x4 i0 = __builtin_bit_cast(i32x4, v0), i1 = __builtin_bit_cast(i32x4, v1);
;                         v0 = (f32x4){(float)i0[0], (float)i0[1], (float)i0[2], (float)i0[3]} * c0; v1 = (f32x4){(float)i1[0], (float)i1[1], (float)i1[2], (float)i1[3]} * c1; }
;                     else if (MODE == 0) { v0 = v0 * tsc; v1 = v1 * tsc; }
;                     if (!QI8 && MODE == 1) { v0 = v0 * cb[bj][0]; v1 = v1 * cb[bj][1]; }
;                     if (MODE == 2 || MODE == 3) { const u32x4 g = gq[kb & 1][bj];
;                         f32x4 g0 = {sigmoidf_(bflo(g.x)), sigmoidf_(bfhi(g.x)), sigmoidf_(bflo(g.y)), sigmoidf_(bfhi(g.y))};
;                         f32x4 g1 = {sigmoidf_(bflo(g.z)), sigmoidf_(bfhi(g.z)), sigmoidf_(bflo(g.w)), sigmoidf_(bfhi(g.w))};
;                         v0 = v0 * g0; v1 = v1 * g1;
;                         if (MODE == 3) { const u32x4 q = aq[kb & 1][bj];
;                             v0 = v0 + (f32x4){bflo(q.x), bfhi(q.x), bflo(q.y), bfhi(q.y)}; v1 = v1 + (f32x4){bflo(q.z), bfhi(q.z), bflo(q.w), bfhi(q.w)}; } }
;                     if (MODE == 4) { v0 = v0 + rs[kb & 1][bj][0]; v1 = v1 + rs[kb & 1][bj][1]; }
;                     if (MODE == 5) { const u32x4 c = gq[kb & 1][bj], q = aq[kb & 1][bj];
;                         v0 = (f32x4){bflo(c.x) + sigmoidf_(v0[0]) * bflo(q.x), bfhi(c.x) + sigmoidf_(v0[1]) * bfhi(q.x), bflo(c.y) + sigmoidf_(v0[2]) * bflo(q.y), bfhi(c.y) + sigmoidf_(v0[3]) * bfhi(q.y)};
;                         v1 = (f32x4){bflo(c.z) + sigmoidf_(v1[0]) * bflo(q.z), bfhi(c.z) + sigmoidf_(v1[1]) * bfhi(q.z), bflo(c.w) + sigmoidf_(v1[2]) * bflo(q.w), bfhi(c.w) + sigmoidf_(v1[3]) * bfhi(q.w)}; }
.LBB0_1038:
	s_or_b64 exec, exec, s[34:35]
	v_or_b32_e32 v114, 16, v130
	v_ashrrev_i32_e32 v115, 31, v114
	s_waitcnt lgkmcnt(0)
	v_mov_b64_e32 v[82:83], s[14:15]
	v_lshlrev_b64 v[84:85], 13, v[114:115]
	v_mad_i64_i32 v[82:83], s[34:35], v114, s65, v[82:83]
	v_lshl_add_u64 v[84:85], s[0:1], 0, v[84:85]
	v_lshl_add_u64 v[82:83], v[82:83], 0, v[166:167]
	v_lshl_add_u64 v[84:85], v[84:85], 0, v[166:167]
	global_load_dwordx4 v[94:97], v[82:83], off nt
	global_load_dwordx4 v[86:89], v[82:83], off offset:256 nt
	global_load_dwordx4 v[90:93], v[84:85], off
	s_nop 0
	global_load_dwordx4 v[82:85], v[84:85], off offset:256
	v_cvt_f32_i32_e32 v81, v81
	v_cvt_f32_i32_e32 v80, v80
	v_pk_mul_f32 v[118:119], v[172:173], v[68:69] op_sel_hi:[0,1]
	v_cvt_f32_i32_e32 v79, v79
	v_cvt_f32_i32_e32 v78, v78
	v_pk_mul_f32 v[80:81], v[118:119], v[80:81]
	s_waitcnt vmcnt(9)
	v_lshlrev_b32_e32 v118, 16, v110
	v_and_b32_e32 v110, 0xffff0000, v110
	v_mul_f32_e32 v118, 0xbfb8aa3b, v118
	v_mul_f32_e32 v110, 0xbfb8aa3b, v110
	v_exp_f32_e32 v118, v118
	v_exp_f32_e32 v119, v110
	v_pk_mul_f32 v[120:121], v[172:173], v[66:67] op_sel_hi:[0,1]
	v_pk_mul_f32 v[78:79], v[120:121], v[78:79]
	v_add_f32_e32 v110, 1.0, v118
	v_add_f32_e32 v118, 1.0, v119
	v_lshlrev_b32_e32 v119, 16, v111
	v_and_b32_e32 v111, 0xffff0000, v111
	v_mul_f32_e32 v119, 0xbfb8aa3b, v119
	v_mul_f32_e32 v111, 0xbfb8aa3b, v111
	v_exp_f32_e32 v119, v119
	v_exp_f32_e32 v120, v111
	v_rcp_f32_e32 v111, v118
	v_cvt_f32_i32_e32 v77, v77
	v_add_f32_e32 v118, 1.0, v119
	v_add_f32_e32 v119, 1.0, v120
	v_lshlrev_b32_e32 v120, 16, v112
	v_and_b32_e32 v112, 0xffff0000, v112
	v_mul_f32_e32 v120, 0xbfb8aa3b, v120
	v_mul_f32_e32 v112, 0xbfb8aa3b, v112
	v_exp_f32_e32 v120, v120
	v_exp_f32_e32 v121, v112
	v_cvt_f32_i32_e32 v76, v76
	v_pk_mul_f32 v[122:123], v[172:173], v[64:65] op_sel_hi:[0,1]
	v_add_f32_e32 v112, 1.0, v120
	v_add_f32_e32 v120, 1.0, v121
	v_lshlrev_b32_e32 v121, 16, v113
	v_and_b32_e32 v113, 0xffff0000, v113
	v_mul_f32_e32 v121, 0xbfb8aa3b, v121
	v_mul_f32_e32 v113, 0xbfb8aa3b, v113
	v_pk_mul_f32 v[76:77], v[122:123], v[76:77]
	v_exp_f32_e32 v121, v121
	v_exp_f32_e32 v122, v113
	v_cvt_f32_i32_e32 v75, v75
	v_cvt_f32_i32_e32 v74, v74
	v_rcp_f32_e32 v110, v110
	v_rcp_f32_e32 v118, v118
	v_rcp_f32_e32 v119, v119
	v_rcp_f32_e32 v113, v120
	v_add_f32_e32 v120, 1.0, v121
	v_add_f32_e32 v121, 1.0, v122
	v_rcp_f32_e32 v112, v112
	v_rcp_f32_e32 v120, v120
	v_rcp_f32_e32 v121, v121
	v_pk_mul_f32 v[124:125], v[172:173], v[62:63] op_sel_hi:[0,1]
	s_waitcnt vmcnt(7)
	v_lshlrev_b32_e32 v122, 16, v106
	v_and_b32_e32 v123, 0xffff0000, v106
	v_lshlrev_b32_e32 v106, 16, v107
	v_and_b32_e32 v107, 0xffff0000, v107
	v_lshlrev_b64 v[116:117], 12, v[130:131]
	v_pk_mul_f32 v[74:75], v[124:125], v[74:75]
	v_pk_fma_f32 v[80:81], v[80:81], v[118:119], v[106:107]
	v_pk_fma_f32 v[78:79], v[78:79], v[110:111], v[122:123]
	v_lshlrev_b32_e32 v106, 16, v108
	v_and_b32_e32 v107, 0xffff0000, v108
	v_lshlrev_b32_e32 v108, 16, v109
	v_and_b32_e32 v109, 0xffff0000, v109
	v_pk_fma_f32 v[108:109], v[76:77], v[120:121], v[108:109]
	v_pk_fma_f32 v[76:77], v[74:75], v[112:113], v[106:107]
	v_cvt_pk_bf16_f32 v74, v78, v79
	v_lshl_add_u64 v[78:79], v[116:117], 1, s[12:13]
	v_lshl_add_u64 v[78:79], v[78:79], 0, v[166:167]
	v_cvt_pk_bf16_f32 v75, v80, v81
	v_cvt_pk_bf16_f32 v76, v76, v77
	v_cvt_pk_bf16_f32 v77, v108, v109
	global_store_dwordx4 v[78:79], v[74:77], off
	v_lshlrev_b32_e32 v80, 16, v74
	v_max_f32_e64 v80, |v80|, |v80|
	v_and_b32_e32 v74, 0xffff0000, v74
	v_max_f32_e64 v74, |v74|, |v74|
	v_max_f32_e32 v74, v80, v74
	v_lshlrev_b32_e32 v80, 16, v75
	v_and_b32_e32 v75, 0xffff0000, v75
	v_lshlrev_b32_e32 v81, 16, v77
	v_and_b32_e32 v77, 0xffff0000, v77
	v_max_f32_e64 v75, |v75|, |v75|
	v_max_f32_e64 v80, |v80|, |v80|
	v_max_f32_e64 v77, |v77|, |v77|
	v_max_f32_e64 v81, |v81|, |v81|
	v_cvt_f32_i32_e32 v73, v73
	v_cvt_f32_i32_e32 v72, v72
	v_max_f32_e32 v75, v80, v75
	v_lshlrev_b32_e32 v80, 16, v76
	v_and_b32_e32 v76, 0xffff0000, v76
	v_max_f32_e32 v77, v81, v77
	v_cvt_f32_i32_e32 v71, v71
	v_cvt_f32_i32_e32 v70, v70
	v_cvt_f32_i32_e32 v61, v61
	v_cvt_f32_i32_e32 v60, v60
	v_max3_f32 v76, |v80|, |v76|, v77
	v_max3_f32 v108, v74, v75, v76
	v_pk_mul_f32 v[74:75], v[172:173], v[56:57] op_sel_hi:[0,1]
	v_pk_mul_f32 v[76:77], v[172:173], v[54:55] op_sel_hi:[0,1]
	v_pk_mul_f32 v[80:81], v[172:173], v[52:53] op_sel_hi:[0,1]
	v_pk_mul_f32 v[72:73], v[74:75], v[72:73]
	v_lshlrev_b32_e32 v74, 16, v102
	v_and_b32_e32 v75, 0xffff0000, v102
	v_pk_mul_f32 v[70:71], v[76:77], v[70:71]
	v_mul_f32_e32 v74, 0xbfb8aa3b, v74
	v_mul_f32_e32 v75, 0xbfb8aa3b, v75
	v_pk_mul_f32 v[60:61], v[80:81], v[60:61]
	v_lshlrev_b32_e32 v76, 16, v103
	v_and_b32_e32 v77, 0xffff0000, v103
	v_lshlrev_b32_e32 v80, 16, v104
	v_and_b32_e32 v81, 0xffff0000, v104
	v_exp_f32_e32 v74, v74
	v_exp_f32_e32 v75, v75
	v_mul_f32_e32 v76, 0xbfb8aa3b, v76
	v_mul_f32_e32 v77, 0xbfb8aa3b, v77
	v_mul_f32_e32 v80, 0xbfb8aa3b, v80
	v_mul_f32_e32 v81, 0xbfb8aa3b, v81
	v_exp_f32_e32 v76, v76
	v_exp_f32_e32 v77, v77
	v_exp_f32_e32 v80, v80
	v_exp_f32_e32 v81, v81
	v_lshlrev_b32_e32 v102, 16, v105
	v_and_b32_e32 v103, 0xffff0000, v105
	v_mul_f32_e32 v102, 0xbfb8aa3b, v102
	v_mul_f32_e32 v103, 0xbfb8aa3b, v103
	v_exp_f32_e32 v102, v102
	v_exp_f32_e32 v103, v103
	v_add_f32_e32 v74, 1.0, v74
	v_add_f32_e32 v75, 1.0, v75
	v_cvt_f32_i32_e32 v59, v59
	v_cvt_f32_i32_e32 v58, v58
	v_rcp_f32_e32 v74, v74
	v_rcp_f32_e32 v75, v75
	v_add_f32_e32 v76, 1.0, v76
	v_add_f32_e32 v77, 1.0, v77
	v_add_f32_e32 v80, 1.0, v80
	v_add_f32_e32 v81, 1.0, v81
	v_rcp_f32_e32 v76, v76
	v_rcp_f32_e32 v77, v77
	v_rcp_f32_e32 v80, v80
	v_rcp_f32_e32 v81, v81
	v_add_f32_e32 v102, 1.0, v102
	v_add_f32_e32 v103, 1.0, v103
	v_pk_mul_f32 v[106:107], v[172:173], v[50:51] op_sel_hi:[0,1]
	v_rcp_f32_e32 v102, v102
	v_rcp_f32_e32 v103, v103
	s_waitcnt vmcnt(7)
;     __device__ __forceinline__ void operator()(const f32x4 (&acc)[2][2][4][2], const Unit& u, int wr, int wc, int fr, int fq) const {
;     ...
;         EPB_LOAD(0);
; #pragma unroll
;         for (int kb = 0; kb < 8; ++kb) { const int ai = kb >> 2, m = kb & 3;
;             if (kb < 7) EPB_LOAD(kb + 1);
;             { const int row = row0 + ai * HALF + m * 16; float rmx = 0.f;
; #pragma unroll
;                 for (int bj = 0; bj < 2; ++bj) { const int col = col0 + bj * HALF; f32x4 v0 = acc[ai][bj][m][0], v1 = acc[ai][bj][m][1];
;                     if (QI8) { const f32x4 c0 = cb[bj][0] * ra[ai][m], c1 = cb[bj][1] * ra[ai][m]; const i32x4 i0 = __builtin_bit_cast(i32x4, v0), i1 = __builtin_bit_cast(i32x4, v1);
;                         v0 = (f32x4){(float)i0[0], (float)i0[1], (float)i0[2], (float)i0[3]} * c0; v1 = (f32x4){(float)i1[0], (float)i1[1], (float)i1[2], (float)i1[3]} * c1; }
;                     else if (MODE == 0) { v0 = v0 * tsc; v1 = v1 * tsc; }
;                     if (!QI8 && MODE == 1) { v0 = v0 * cb[bj][0]; v1 = v1 * cb[bj][1]; }
;                     if (MODE == 2 || MODE == 3) { const u32x4 g = gq[kb & 1][bj];
;                         f32x4 g0 = {sigmoidf_(bflo(g.x)), sigmoidf_(bfhi(g.x)), sigmoidf_(bflo(g.y)), sigmoidf_(bfhi(g.y))};
;                         f32x4 g1 = {sigmoidf_(bflo(g.z)), sigmoidf_(bfhi(g.z)), sigmoidf_(bflo(g.w)), sigmoidf_(bfhi(g.w))};
;                         v0 = v0 * g0; v1 = v1 * g1;
;                         if (MODE == 3) { const u32x4 q = aq[kb & 1][bj];
;                             v0 = v0 + (f32x4){bflo(q.x), bfhi(q.x), bflo(q.y), bfhi(q.y)}; v1 = v1 + (f32x4){bflo(q.z), bfhi(q.z), bflo(q.w), bfhi(q.w)}; } }
;                     if (MODE == 4) { v0 = v0 + rs[kb & 1][bj][0]; v1 = v1 + rs[kb & 1][bj][1]; }
;                     if (MODE == 5) { const u32x4 c = gq[kb & 1][bj], q = aq[kb & 1][bj];
;                         v0 = (f32x4){bflo(c.x) + sigmoidf_(v0[0]) * bflo(q.x), bfhi(c.x) + sigmoidf_(v0[1]) * bfhi(q.x), bflo(c.y) + sigmoidf_(v0[2]) * bflo(q.y), bfhi(c.y) + sigmoidf_(v0[3]) * bfhi(q.y)};
;                         v1 = (f32x4){bflo(c.z) + sigmoidf_(v1[0]) * bflo(q.z), bfhi(c.z) + sigmoidf_(v1[1]) * bfhi(q.z), bflo(c.w) + sigmoidf_(v1[2]) * bflo(q.w), bfhi(c.w) + sigmoidf_(v1[3]) * bfhi(q.w)}; }
	v_lshlrev_b32_e32 v104, 16, v98
	v_and_b32_e32 v105, 0xffff0000, v98
	v_pk_mul_f32 v[58:59], v[106:107], v[58:59]
	v_lshlrev_b32_e32 v98, 16, v99
	v_and_b32_e32 v99, 0xffff0000, v99
	v_pk_fma_f32 v[70:71], v[70:71], v[74:75], v[104:105]
	v_lshlrev_b32_e32 v74, 16, v100
	v_and_b32_e32 v75, 0xffff0000, v100
	v_pk_fma_f32 v[72:73], v[72:73], v[76:77], v[98:99]
	v_pk_fma_f32 v[58:59], v[58:59], v[80:81], v[74:75]
	v_lshlrev_b32_e32 v76, 16, v101
	v_and_b32_e32 v77, 0xffff0000, v101
	v_cvt_pk_bf16_f32 v70, v70, v71
	v_cvt_pk_bf16_f32 v71, v72, v73
	v_cvt_pk_bf16_f32 v72, v58, v59
	v_pk_fma_f32 v[60:61], v[60:61], v[102:103], v[76:77]
	v_lshlrev_b32_e32 v58, 16, v70
	v_and_b32_e32 v59, 0xffff0000, v70
	v_max_f32_e64 v59, |v59|, |v59|
	v_max_f32_e64 v58, |v58|, |v58|
	v_cvt_pk_bf16_f32 v73, v60, v61
	v_max_f32_e32 v58, v58, v59
	v_lshlrev_b32_e32 v59, 16, v71
	v_and_b32_e32 v60, 0xffff0000, v71
	v_lshlrev_b32_e32 v74, 16, v73
	v_and_b32_e32 v75, 0xffff0000, v73
	v_max_f32_e64 v60, |v60|, |v60|
	v_max_f32_e64 v59, |v59|, |v59|
	v_max_f32_e64 v75, |v75|, |v75|
	v_max_f32_e64 v74, |v74|, |v74|
	v_max_f32_e32 v59, v59, v60
	v_lshlrev_b32_e32 v60, 16, v72
	v_and_b32_e32 v61, 0xffff0000, v72
	v_max_f32_e32 v74, v74, v75
	v_max3_f32 v60, |v60|, |v61|, v74
	v_max3_f32 v58, v58, v59, v60
	v_max3_f32 v58, v108, 0, v58
	ds_bpermute_b32 v59, v165, v58
	global_store_dwordx4 v[78:79], v[70:73], off offset:256
	s_waitcnt lgkmcnt(0)
	v_max_f32_e32 v59, v59, v59
	v_max_f32_e32 v58, v58, v59
	ds_bpermute_b32 v59, v169, v58
	s_and_saveexec_b64 s[34:35], s[6:7]
	s_cbranch_execz .LBB0_1040
	s_waitcnt lgkmcnt(0)
	v_max_f32_e32 v59, v59, v59
	v_max_f32_e32 v58, v58, v58
	v_lshl_add_u64 v[60:61], v[130:131], 2, s[16:17]
	v_max_f32_e32 v58, v58, v59
	global_atomic_umax v[60:61], v58, off
.LBB0_1040:
	s_or_b64 exec, exec, s[34:35]
	v_or_b32_e32 v98, 32, v130
	v_ashrrev_i32_e32 v99, 31, v98
	s_waitcnt lgkmcnt(0)
	v_mov_b64_e32 v[58:59], s[14:15]
	v_lshlrev_b64 v[60:61], 13, v[98:99]
	v_mad_i64_i32 v[58:59], s[34:35], v98, s65, v[58:59]
	v_lshl_add_u64 v[60:61], s[0:1], 0, v[60:61]
	v_lshl_add_u64 v[58:59], v[58:59], 0, v[166:167]
	v_lshl_add_u64 v[60:61], v[60:61], 0, v[166:167]
	global_load_dwordx4 v[78:81], v[58:59], off nt
	global_load_dwordx4 v[70:73], v[58:59], off offset:256 nt
	global_load_dwordx4 v[74:77], v[60:61], off
	s_nop 0
	global_load_dwordx4 v[58:61], v[60:61], off offset:256
	v_cvt_f32_i32_e32 v49, v49
	v_cvt_f32_i32_e32 v48, v48
	v_pk_mul_f32 v[102:103], v[170:171], v[68:69] op_sel_hi:[0,1]
	v_cvt_f32_i32_e32 v47, v47
	v_cvt_f32_i32_e32 v46, v46
	v_pk_mul_f32 v[48:49], v[102:103], v[48:49]
	s_waitcnt vmcnt(9)
	v_lshlrev_b32_e32 v102, 16, v94
	v_and_b32_e32 v94, 0xffff0000, v94
	v_mul_f32_e32 v102, 0xbfb8aa3b, v102
	v_mul_f32_e32 v94, 0xbfb8aa3b, v94
	v_exp_f32_e32 v102, v102
	v_exp_f32_e32 v103, v94
	v_pk_mul_f32 v[104:105], v[170:171], v[66:67] op_sel_hi:[0,1]
	v_pk_mul_f32 v[46:47], v[104:105], v[46:47]
	v_add_f32_e32 v94, 1.0, v102
	v_add_f32_e32 v102, 1.0, v103
	v_lshlrev_b32_e32 v103, 16, v95
	v_and_b32_e32 v95, 0xffff0000, v95
	v_mul_f32_e32 v103, 0xbfb8aa3b, v103
	v_mul_f32_e32 v95, 0xbfb8aa3b, v95
	v_exp_f32_e32 v103, v103
	v_exp_f32_e32 v104, v95
	v_rcp_f32_e32 v95, v102
	v_cvt_f32_i32_e32 v45, v45
	v_add_f32_e32 v102, 1.0, v103
	v_add_f32_e32 v103, 1.0, v104
	v_lshlrev_b32_e32 v104, 16, v96
	v_and_b32_e32 v96, 0xffff0000, v96
	v_mul_f32_e32 v104, 0xbfb8aa3b, v104
	v_mul_f32_e32 v96, 0xbfb8aa3b, v96
	v_exp_f32_e32 v104, v104
	v_exp_f32_e32 v105, v96
	v_cvt_f32_i32_e32 v44, v44
	v_pk_mul_f32 v[106:107], v[170:171], v[64:65] op_sel_hi:[0,1]
	v_add_f32_e32 v96, 1.0, v104
	v_add_f32_e32 v104, 1.0, v105
	v_lshlrev_b32_e32 v105, 16, v97
	v_and_b32_e32 v97, 0xffff0000, v97
	v_mul_f32_e32 v105, 0xbfb8aa3b, v105
	v_mul_f32_e32 v97, 0xbfb8aa3b, v97
	v_pk_mul_f32 v[44:45], v[106:107], v[44:45]
	v_exp_f32_e32 v105, v105
	v_exp_f32_e32 v106, v97
	v_cvt_f32_i32_e32 v43, v43
	v_cvt_f32_i32_e32 v42, v42
	v_rcp_f32_e32 v94, v94
	v_rcp_f32_e32 v102, v102
	v_rcp_f32_e32 v103, v103
	v_rcp_f32_e32 v97, v104
	v_add_f32_e32 v104, 1.0, v105
	v_add_f32_e32 v105, 1.0, v106
	v_rcp_f32_e32 v96, v96
	v_rcp_f32_e32 v104, v104
	v_rcp_f32_e32 v105, v105
	v_pk_mul_f32 v[108:109], v[170:171], v[62:63] op_sel_hi:[0,1]
	s_waitcnt vmcnt(7)
;     __device__ __forceinline__ void operator()(const f32x4 (&acc)[2][2][4][2], const Unit& u, int wr, int wc, int fr, int fq) const {
;     ...
;             { const int row = row0 + ai * HALF + m * 16; float rmx = 0.f;
; #pragma unroll
;                 for (int bj = 0; bj < 2; ++bj) { const int col = col0 + bj * HALF; f32x4 v0 = acc[ai][bj][m][0], v1 = acc[ai][bj][m][1];
;                     if (QI8) { const f32x4 c0 = cb[bj][0] * ra[ai][m], c1 = cb[bj][1] * ra[ai][m]; const i32x4 i0 = __builtin_bit_cast(i32x4, v0), i1 = __builtin_bit_cast(i32x4, v1);
;                         v0 = (f32x4){(float)i0[0], (float)i0[1], (float)i0[2], (float)i0[3]} * c0; v1 = (f32x4){(float)i1[0], (float)i1[1], (float)i1[2], (float)i1[3]} * c1; }
;                     else if (MODE == 0) { v0 = v0 * tsc; v1 = v1 * tsc; }
;                     if (!QI8 && MODE == 1) { v0 = v0 * cb[bj][0]; v1 = v1 * cb[bj][1]; }
;                     if (MODE == 2 || MODE == 3) { const u32x4 g = gq[kb & 1][bj];
;                         f32x4 g0 = {sigmoidf_(bflo(g.x)), sigmoidf_(bfhi(g.x)), sigmoidf_(bflo(g.y)), sigmoidf_(bfhi(g.y))};
;                         f32x4 g1 = {sigmoidf_(bflo(g.z)), sigmoidf_(bfhi(g.z)), sigmoidf_(bflo(g.w)), sigmoidf_(bfhi(g.w))};
;                         v0 = v0 * g0; v1 = v1 * g1;
;                         if (MODE == 3) { const u32x4 q = aq[kb & 1][bj];
;                             v0 = v0 + (f32x4){bflo(q.x), bfhi(q.x), bflo(q.y), bfhi(q.y)}; v1 = v1 + (f32x4){bflo(q.z), bfhi(q.z), bflo(q.w), bfhi(q.w)}; } }
;                     if (MODE == 4) { v0 = v0 + rs[kb & 1][bj][0]; v1 = v1 + rs[kb & 1][bj][1]; }
;                     if (MODE == 5) { const u32x4 c = gq[kb & 1][bj], q = aq[kb & 1][bj];
;                         v0 = (f32x4){bflo(c.x) + sigmoidf_(v0[0]) * bflo(q.x), bfhi(c.x) + sigmoidf_(v0[1]) * bfhi(q.x), bflo(c.y) + sigmoidf_(v0[2]) * bflo(q.y), bfhi(c.y) + sigmoidf_(v0[3]) * bfhi(q.y)};
;                         v1 = (f32x4){bflo(c.z) + sigmoidf_(v1[0]) * bflo(q.z), bfhi(c.z) + sigmoidf_(v1[1]) * bfhi(q.z), bflo(c.w) + sigmoidf_(v1[2]) * bflo(q.w), bfhi(c.w) + sigmoidf_(v1[3]) * bfhi(q.w)}; }
;                     u32x4 w; w.x = cvtpk(v0[0], v0[1]); w.y = cvtpk(v0[2], v0[3]); w.z = cvtpk(v1[0], v1[1]); w.w = cvtpk(v1[2], v1[3]);
;                     *(u32x4*)(O + (size_t)row * ldo + col) = w;
	v_lshlrev_b32_e32 v106, 16, v90
	v_and_b32_e32 v107, 0xffff0000, v90
	v_lshlrev_b32_e32 v90, 16, v91
	v_and_b32_e32 v91, 0xffff0000, v91
	v_lshlrev_b64 v[100:101], 12, v[114:115]
	v_pk_mul_f32 v[42:43], v[108:109], v[42:43]
	v_pk_fma_f32 v[48:49], v[48:49], v[102:103], v[90:91]
	v_pk_fma_f32 v[46:47], v[46:47], v[94:95], v[106:107]
	v_lshlrev_b32_e32 v90, 16, v92
	v_and_b32_e32 v91, 0xffff0000, v92
	v_lshlrev_b32_e32 v92, 16, v93
	v_and_b32_e32 v93, 0xffff0000, v93
	v_pk_fma_f32 v[92:93], v[44:45], v[104:105], v[92:93]
	v_pk_fma_f32 v[44:45], v[42:43], v[96:97], v[90:91]
	v_cvt_pk_bf16_f32 v42, v46, v47
	v_lshl_add_u64 v[46:47], v[100:101], 1, s[12:13]
	v_lshl_add_u64 v[46:47], v[46:47], 0, v[166:167]
	v_cvt_pk_bf16_f32 v43, v48, v49
	v_cvt_pk_bf16_f32 v44, v44, v45
	v_cvt_pk_bf16_f32 v45, v92, v93
	global_store_dwordx4 v[46:47], v[42:45], off
	v_lshlrev_b32_e32 v48, 16, v42
	v_max_f32_e64 v48, |v48|, |v48|
	v_and_b32_e32 v42, 0xffff0000, v42
	v_max_f32_e64 v42, |v42|, |v42|
	v_max_f32_e32 v42, v48, v42
	v_lshlrev_b32_e32 v48, 16, v43
	v_and_b32_e32 v43, 0xffff0000, v43
	v_lshlrev_b32_e32 v49, 16, v45
	v_and_b32_e32 v45, 0xffff0000, v45
	v_max_f32_e64 v43, |v43|, |v43|
	v_max_f32_e64 v48, |v48|, |v48|
	v_max_f32_e64 v45, |v45|, |v45|
	v_max_f32_e64 v49, |v49|, |v49|
	v_cvt_f32_i32_e32 v41, v41
	v_cvt_f32_i32_e32 v40, v40
	v_max_f32_e32 v43, v48, v43
	v_lshlrev_b32_e32 v48, 16, v44
	v_and_b32_e32 v44, 0xffff0000, v44
	v_max_f32_e32 v45, v49, v45
	v_cvt_f32_i32_e32 v39, v39
	v_cvt_f32_i32_e32 v38, v38
	v_cvt_f32_i32_e32 v37, v37
	v_cvt_f32_i32_e32 v36, v36
	v_max3_f32 v44, |v48|, |v44|, v45
	v_max3_f32 v92, v42, v43, v44
	v_pk_mul_f32 v[42:43], v[170:171], v[56:57] op_sel_hi:[0,1]
	v_pk_mul_f32 v[44:45], v[170:171], v[54:55] op_sel_hi:[0,1]
	v_pk_mul_f32 v[48:49], v[170:171], v[52:53] op_sel_hi:[0,1]
	v_pk_mul_f32 v[40:41], v[42:43], v[40:41]
	v_lshlrev_b32_e32 v42, 16, v86
	v_and_b32_e32 v43, 0xffff0000, v86
	v_pk_mul_f32 v[38:39], v[44:45], v[38:39]
	v_mul_f32_e32 v42, 0xbfb8aa3b, v42
	v_mul_f32_e32 v43, 0xbfb8aa3b, v43
	v_pk_mul_f32 v[36:37], v[48:49], v[36:37]
	v_lshlrev_b32_e32 v44, 16, v87
	v_and_b32_e32 v45, 0xffff0000, v87
	v_lshlrev_b32_e32 v48, 16, v88
	v_and_b32_e32 v49, 0xffff0000, v88
	v_exp_f32_e32 v42, v42
	v_exp_f32_e32 v43, v43
	v_mul_f32_e32 v44, 0xbfb8aa3b, v44
	v_mul_f32_e32 v45, 0xbfb8aa3b, v45
	v_mul_f32_e32 v48, 0xbfb8aa3b, v48
	v_mul_f32_e32 v49, 0xbfb8aa3b, v49
	v_lshlrev_b32_e32 v86, 16, v89
	v_and_b32_e32 v87, 0xffff0000, v89
	v_exp_f32_e32 v44, v44
	v_exp_f32_e32 v45, v45
	v_exp_f32_e32 v48, v48
	v_exp_f32_e32 v49, v49
	v_mul_f32_e32 v86, 0xbfb8aa3b, v86
	v_mul_f32_e32 v87, 0xbfb8aa3b, v87
	v_exp_f32_e32 v86, v86
	v_exp_f32_e32 v87, v87
	v_add_f32_e32 v42, 1.0, v42
	v_add_f32_e32 v43, 1.0, v43
	v_cvt_f32_i32_e32 v35, v35
	v_cvt_f32_i32_e32 v34, v34
	v_rcp_f32_e32 v42, v42
	v_rcp_f32_e32 v43, v43
	v_add_f32_e32 v44, 1.0, v44
	v_add_f32_e32 v45, 1.0, v45
	v_add_f32_e32 v48, 1.0, v48
	v_add_f32_e32 v49, 1.0, v49
	v_rcp_f32_e32 v44, v44
	v_rcp_f32_e32 v45, v45
	v_rcp_f32_e32 v48, v48
	v_rcp_f32_e32 v49, v49
	v_add_f32_e32 v86, 1.0, v86
	v_add_f32_e32 v87, 1.0, v87
	v_rcp_f32_e32 v86, v86
	v_rcp_f32_e32 v87, v87
	v_pk_mul_f32 v[90:91], v[170:171], v[50:51] op_sel_hi:[0,1]
	s_waitcnt vmcnt(7)
	v_lshlrev_b32_e32 v88, 16, v82
	v_and_b32_e32 v89, 0xffff0000, v82
	v_pk_mul_f32 v[34:35], v[90:91], v[34:35]
	v_lshlrev_b32_e32 v82, 16, v83
	v_and_b32_e32 v83, 0xffff0000, v83
	v_pk_fma_f32 v[38:39], v[38:39], v[42:43], v[88:89]
	v_lshlrev_b32_e32 v42, 16, v84
	v_and_b32_e32 v43, 0xffff0000, v84
	v_pk_fma_f32 v[40:41], v[40:41], v[44:45], v[82:83]
	v_lshlrev_b32_e32 v44, 16, v85
	v_and_b32_e32 v45, 0xffff0000, v85
	v_pk_fma_f32 v[34:35], v[34:35], v[48:49], v[42:43]
	v_pk_fma_f32 v[44:45], v[36:37], v[86:87], v[44:45]
	v_cvt_pk_bf16_f32 v36, v38, v39
	v_cvt_pk_bf16_f32 v37, v40, v41
	v_cvt_pk_bf16_f32 v38, v34, v35
	s_nop 0
	v_lshlrev_b32_e32 v34, 16, v36
	v_and_b32_e32 v35, 0xffff0000, v36
	v_max_f32_e64 v35, |v35|, |v35|
	v_max_f32_e64 v34, |v34|, |v34|
	v_cvt_pk_bf16_f32 v39, v44, v45
	v_max_f32_e32 v34, v34, v35
	v_lshlrev_b32_e32 v35, 16, v37
	v_and_b32_e32 v40, 0xffff0000, v37
	v_lshlrev_b32_e32 v42, 16, v39
	v_and_b32_e32 v43, 0xffff0000, v39
	v_max_f32_e64 v40, |v40|, |v40|
	v_max_f32_e64 v35, |v35|, |v35|
	v_max_f32_e64 v43, |v43|, |v43|
	v_max_f32_e64 v42, |v42|, |v42|
	v_max_f32_e32 v35, v35, v40
	v_lshlrev_b32_e32 v40, 16, v38
	v_and_b32_e32 v41, 0xffff0000, v38
	v_max_f32_e32 v42, v42, v43
	v_max3_f32 v40, |v40|, |v41|, v42
	v_max3_f32 v34, v34, v35, v40
	v_max3_f32 v34, v92, 0, v34
	ds_bpermute_b32 v35, v165, v34
	global_store_dwordx4 v[46:47], v[36:39], off offset:256
	s_waitcnt lgkmcnt(0)
	v_max_f32_e32 v35, v35, v35
	v_max_f32_e32 v34, v34, v35
	ds_bpermute_b32 v35, v169, v34
	s_and_saveexec_b64 s[34:35], s[6:7]
	s_cbranch_execz .LBB0_1042
	s_waitcnt lgkmcnt(0)
	v_max_f32_e32 v35, v35, v35
	v_max_f32_e32 v34, v34, v34
	v_lshl_add_u64 v[36:37], v[114:115], 2, s[16:17]
	v_max_f32_e32 v34, v34, v35
	global_atomic_umax v[36:37], v34, off
; __device__ __forceinline__ float sigmoidf_(float x) { return __builtin_amdgcn_rcpf(1.f + __builtin_amdgcn_exp2f(-1.4426950408889634f * x)); }
;     __device__ __forceinline__ void operator()(const f32x4 (&acc)[2][2][4][2], const Unit& u, int wr, int wc, int fr, int fq) const {
;     ...
;         EPB_LOAD(0);
; #pragma unroll
;         for (int kb = 0; kb < 8; ++kb) { const int ai = kb >> 2, m = kb & 3;
;             if (kb < 7) EPB_LOAD(kb + 1);
;             { const int row = row0 + ai * HALF + m * 16; float rmx = 0.f;
; #pragma unroll
;                 for (int bj = 0; bj < 2; ++bj) { const int col = col0 + bj * HALF; f32x4 v0 = acc[ai][bj][m][0], v1 = acc[ai][bj][m][1];
;                     if (QI8) { const f32x4 c0 = cb[bj][0] * ra[ai][m], c1 = cb[bj][1] * ra[ai][m]; const i32x4 i0 = __builtin_bit_cast(i32x4, v0), i1 = __builtin_bit_cast(i32x4, v1);
;                         v0 = (f32x4){(float)i0[0], (float)i0[1], (float)i0[2], (float)i0[3]} * c0; v1 = (f32x4){(float)i1[0], (float)i1[1], (float)i1[2], (float)i1[3]} * c1; }
;                     else if (MODE == 0) { v0 = v0 * tsc; v1 = v1 * tsc; }
;                     if (!QI8 && MODE == 1) { v0 = v0 * cb[bj][0]; v1 = v1 * cb[bj][1]; }
;                     if (MODE == 2 || MODE == 3) { const u32x4 g = gq[kb & 1][bj];
;                         f32x4 g0 = {sigmoidf_(bflo(g.x)), sigmoidf_(bfhi(g.x)), sigmoidf_(bflo(g.y)), sigmoidf_(bfhi(g.y))};
;                         f32x4 g1 = {sigmoidf_(bflo(g.z)), sigmoidf_(bfhi(g.z)), sigmoidf_(bflo(g.w)), sigmoidf_(bfhi(g.w))};
;                         v0 = v0 * g0; v1 = v1 * g1;
;                         if (MODE == 3) { const u32x4 q = aq[kb & 1][bj];
;                             v0 = v0 + (f32x4){bflo(q.x), bfhi(q.x), bflo(q.y), bfhi(q.y)}; v1 = v1 + (f32x4){bflo(q.z), bfhi(q.z), bflo(q.w), bfhi(q.w)}; } }
.LBB0_1042:
	s_or_b64 exec, exec, s[34:35]
	v_or_b32_e32 v82, 48, v130
	v_ashrrev_i32_e32 v83, 31, v82
	s_waitcnt lgkmcnt(0)
	v_mov_b64_e32 v[34:35], s[14:15]
	v_lshlrev_b64 v[36:37], 13, v[82:83]
	v_mad_i64_i32 v[34:35], s[34:35], v82, s65, v[34:35]
	v_lshl_add_u64 v[36:37], s[0:1], 0, v[36:37]
	v_lshl_add_u64 v[34:35], v[34:35], 0, v[166:167]
	v_lshl_add_u64 v[36:37], v[36:37], 0, v[166:167]
	global_load_dwordx4 v[46:49], v[34:35], off nt
	global_load_dwordx4 v[38:41], v[34:35], off offset:256 nt
	global_load_dwordx4 v[42:45], v[36:37], off
	s_nop 0
	global_load_dwordx4 v[34:37], v[36:37], off offset:256
	v_cvt_f32_i32_e32 v33, v33
	v_cvt_f32_i32_e32 v32, v32
	v_pk_mul_f32 v[86:87], v[168:169], v[68:69] op_sel_hi:[0,1]
	v_cvt_f32_i32_e32 v31, v31
	v_cvt_f32_i32_e32 v30, v30
	v_pk_mul_f32 v[32:33], v[86:87], v[32:33]
	s_waitcnt vmcnt(9)
	v_lshlrev_b32_e32 v86, 16, v78
	v_and_b32_e32 v78, 0xffff0000, v78
	v_mul_f32_e32 v86, 0xbfb8aa3b, v86
	v_mul_f32_e32 v78, 0xbfb8aa3b, v78
	v_exp_f32_e32 v86, v86
	v_exp_f32_e32 v87, v78
	v_pk_mul_f32 v[88:89], v[168:169], v[66:67] op_sel_hi:[0,1]
	v_pk_mul_f32 v[30:31], v[88:89], v[30:31]
	v_add_f32_e32 v78, 1.0, v86
	v_add_f32_e32 v86, 1.0, v87
	v_lshlrev_b32_e32 v87, 16, v79
	v_and_b32_e32 v79, 0xffff0000, v79
	v_mul_f32_e32 v87, 0xbfb8aa3b, v87
	v_mul_f32_e32 v79, 0xbfb8aa3b, v79
	v_exp_f32_e32 v87, v87
	v_exp_f32_e32 v88, v79
	v_rcp_f32_e32 v79, v86
	v_cvt_f32_i32_e32 v29, v29
	v_add_f32_e32 v86, 1.0, v87
	v_add_f32_e32 v87, 1.0, v88
	v_lshlrev_b32_e32 v88, 16, v80
	v_and_b32_e32 v80, 0xffff0000, v80
	v_mul_f32_e32 v88, 0xbfb8aa3b, v88
	v_mul_f32_e32 v80, 0xbfb8aa3b, v80
	v_exp_f32_e32 v88, v88
	v_exp_f32_e32 v89, v80
	v_cvt_f32_i32_e32 v28, v28
	v_pk_mul_f32 v[90:91], v[168:169], v[64:65] op_sel_hi:[0,1]
	v_add_f32_e32 v80, 1.0, v88
	v_add_f32_e32 v88, 1.0, v89
	v_lshlrev_b32_e32 v89, 16, v81
	v_and_b32_e32 v81, 0xffff0000, v81
	v_mul_f32_e32 v89, 0xbfb8aa3b, v89
	v_mul_f32_e32 v81, 0xbfb8aa3b, v81
	v_pk_mul_f32 v[28:29], v[90:91], v[28:29]
	v_exp_f32_e32 v89, v89
	v_exp_f32_e32 v90, v81
	v_cvt_f32_i32_e32 v27, v27
	v_cvt_f32_i32_e32 v26, v26
	v_rcp_f32_e32 v78, v78
	v_rcp_f32_e32 v86, v86
	v_rcp_f32_e32 v87, v87
	v_rcp_f32_e32 v81, v88
	v_add_f32_e32 v88, 1.0, v89
	v_add_f32_e32 v89, 1.0, v90
	v_rcp_f32_e32 v80, v80
	v_rcp_f32_e32 v88, v88
	v_rcp_f32_e32 v89, v89
	v_pk_mul_f32 v[92:93], v[168:169], v[62:63] op_sel_hi:[0,1]
	s_waitcnt vmcnt(7)
;     __device__ __forceinline__ void operator()(const f32x4 (&acc)[2][2][4][2], const Unit& u, int wr, int wc, int fr, int fq) const {
;     ...
;             { const int row = row0 + ai * HALF + m * 16; float rmx = 0.f;
; #pragma unroll
;                 for (int bj = 0; bj < 2; ++bj) { const int col = col0 + bj * HALF; f32x4 v0 = acc[ai][bj][m][0], v1 = acc[ai][bj][m][1];
;                     if (QI8) { const f32x4 c0 = cb[bj][0] * ra[ai][m], c1 = cb[bj][1] * ra[ai][m]; const i32x4 i0 = __builtin_bit_cast(i32x4, v0), i1 = __builtin_bit_cast(i32x4, v1);
;                         v0 = (f32x4){(float)i0[0], (float)i0[1], (float)i0[2], (float)i0[3]} * c0; v1 = (f32x4){(float)i1[0], (float)i1[1], (float)i1[2], (float)i1[3]} * c1; }
;                     else if (MODE == 0) { v0 = v0 * tsc; v1 = v1 * tsc; }
;                     if (!QI8 && MODE == 1) { v0 = v0 * cb[bj][0]; v1 = v1 * cb[bj][1]; }
;                     if (MODE == 2 || MODE == 3) { const u32x4 g = gq[kb & 1][bj];
;                         f32x4 g0 = {sigmoidf_(bflo(g.x)), sigmoidf_(bfhi(g.x)), sigmoidf_(bflo(g.y)), sigmoidf_(bfhi(g.y))};
;                         f32x4 g1 = {sigmoidf_(bflo(g.z)), sigmoidf_(bfhi(g.z)), sigmoidf_(bflo(g.w)), sigmoidf_(bfhi(g.w))};
;                         v0 = v0 * g0; v1 = v1 * g1;
;                         if (MODE == 3) { const u32x4 q = aq[kb & 1][bj];
;                             v0 = v0 + (f32x4){bflo(q.x), bfhi(q.x), bflo(q.y), bfhi(q.y)}; v1 = v1 + (f32x4){bflo(q.z), bfhi(q.z), bflo(q.w), bfhi(q.w)}; } }
;                     if (MODE == 4) { v0 = v0 + rs[kb & 1][bj][0]; v1 = v1 + rs[kb & 1][bj][1]; }
;                     if (MODE == 5) { const u32x4 c = gq[kb & 1][bj], q = aq[kb & 1][bj];
;                         v0 = (f32x4){bflo(c.x) + sigmoidf_(v0[0]) * bflo(q.x), bfhi(c.x) + sigmoidf_(v0[1]) * bfhi(q.x), bflo(c.y) + sigmoidf_(v0[2]) * bflo(q.y), bfhi(c.y) + sigmoidf_(v0[3]) * bfhi(q.y)};
;                         v1 = (f32x4){bflo(c.z) + sigmoidf_(v1[0]) * bflo(q.z), bfhi(c.z) + sigmoidf_(v1[1]) * bfhi(q.z), bflo(c.w) + sigmoidf_(v1[2]) * bflo(q.w), bfhi(c.w) + sigmoidf_(v1[3]) * bfhi(q.w)}; }
;                     u32x4 w; w.x = cvtpk(v0[0], v0[1]); w.y = cvtpk(v0[2], v0[3]); w.z = cvtpk(v1[0], v1[1]); w.w = cvtpk(v1[2], v1[3]);
;                     *(u32x4*)(O + (size_t)row * ldo + col) = w;
	v_lshlrev_b32_e32 v90, 16, v74
	v_and_b32_e32 v91, 0xffff0000, v74
	v_lshlrev_b32_e32 v74, 16, v75
	v_and_b32_e32 v75, 0xffff0000, v75
	v_lshlrev_b64 v[84:85], 12, v[98:99]
	v_pk_mul_f32 v[26:27], v[92:93], v[26:27]
	v_pk_fma_f32 v[32:33], v[32:33], v[86:87], v[74:75]
	v_pk_fma_f32 v[30:31], v[30:31], v[78:79], v[90:91]
	v_lshlrev_b32_e32 v74, 16, v76
	v_and_b32_e32 v75, 0xffff0000, v76
	v_lshlrev_b32_e32 v76, 16, v77
	v_and_b32_e32 v77, 0xffff0000, v77
	v_pk_fma_f32 v[76:77], v[28:29], v[88:89], v[76:77]
	v_pk_fma_f32 v[28:29], v[26:27], v[80:81], v[74:75]
	v_cvt_pk_bf16_f32 v26, v30, v31
	v_lshl_add_u64 v[30:31], v[84:85], 1, s[12:13]
	v_lshl_add_u64 v[30:31], v[30:31], 0, v[166:167]
	v_cvt_pk_bf16_f32 v27, v32, v33
	v_cvt_pk_bf16_f32 v28, v28, v29
	v_cvt_pk_bf16_f32 v29, v76, v77
	global_store_dwordx4 v[30:31], v[26:29], off
	v_lshlrev_b32_e32 v32, 16, v26
	v_max_f32_e64 v32, |v32|, |v32|
	v_and_b32_e32 v26, 0xffff0000, v26
	v_max_f32_e64 v26, |v26|, |v26|
	v_max_f32_e32 v26, v32, v26
	v_lshlrev_b32_e32 v32, 16, v27
	v_and_b32_e32 v27, 0xffff0000, v27
	v_lshlrev_b32_e32 v33, 16, v29
	v_and_b32_e32 v29, 0xffff0000, v29
	v_max_f32_e64 v27, |v27|, |v27|
	v_max_f32_e64 v32, |v32|, |v32|
	v_max_f32_e64 v29, |v29|, |v29|
	v_max_f32_e64 v33, |v33|, |v33|
	v_cvt_f32_i32_e32 v25, v25
	v_cvt_f32_i32_e32 v24, v24
	v_max_f32_e32 v27, v32, v27
	v_lshlrev_b32_e32 v32, 16, v28
	v_and_b32_e32 v28, 0xffff0000, v28
	v_max_f32_e32 v29, v33, v29
	v_cvt_f32_i32_e32 v23, v23
	v_cvt_f32_i32_e32 v22, v22
	v_cvt_f32_i32_e32 v21, v21
	v_cvt_f32_i32_e32 v20, v20
	v_max3_f32 v28, |v32|, |v28|, v29
	v_max3_f32 v76, v26, v27, v28
	v_pk_mul_f32 v[26:27], v[168:169], v[56:57] op_sel_hi:[0,1]
	v_pk_mul_f32 v[28:29], v[168:169], v[54:55] op_sel_hi:[0,1]
	v_pk_mul_f32 v[32:33], v[168:169], v[52:53] op_sel_hi:[0,1]
	v_pk_mul_f32 v[24:25], v[26:27], v[24:25]
	v_lshlrev_b32_e32 v26, 16, v70
	v_and_b32_e32 v27, 0xffff0000, v70
	v_pk_mul_f32 v[22:23], v[28:29], v[22:23]
	v_mul_f32_e32 v26, 0xbfb8aa3b, v26
	v_mul_f32_e32 v27, 0xbfb8aa3b, v27
	v_pk_mul_f32 v[20:21], v[32:33], v[20:21]
	v_lshlrev_b32_e32 v28, 16, v71
	v_and_b32_e32 v29, 0xffff0000, v71
	v_lshlrev_b32_e32 v32, 16, v72
	v_and_b32_e32 v33, 0xffff0000, v72
	v_exp_f32_e32 v26, v26
	v_exp_f32_e32 v27, v27
	v_mul_f32_e32 v28, 0xbfb8aa3b, v28
	v_mul_f32_e32 v29, 0xbfb8aa3b, v29
	v_mul_f32_e32 v32, 0xbfb8aa3b, v32
	v_mul_f32_e32 v33, 0xbfb8aa3b, v33
	v_lshlrev_b32_e32 v70, 16, v73
	v_and_b32_e32 v71, 0xffff0000, v73
	v_exp_f32_e32 v28, v28
	v_exp_f32_e32 v29, v29
	v_exp_f32_e32 v32, v32
	v_exp_f32_e32 v33, v33
	v_mul_f32_e32 v70, 0xbfb8aa3b, v70
	v_mul_f32_e32 v71, 0xbfb8aa3b, v71
	v_exp_f32_e32 v70, v70
	v_exp_f32_e32 v71, v71
	v_add_f32_e32 v26, 1.0, v26
	v_add_f32_e32 v27, 1.0, v27
	v_cvt_f32_i32_e32 v19, v19
	v_cvt_f32_i32_e32 v18, v18
	v_rcp_f32_e32 v26, v26
	v_rcp_f32_e32 v27, v27
	v_add_f32_e32 v28, 1.0, v28
	v_add_f32_e32 v29, 1.0, v29
	v_add_f32_e32 v32, 1.0, v32
	v_add_f32_e32 v33, 1.0, v33
	v_rcp_f32_e32 v28, v28
	v_rcp_f32_e32 v29, v29
	v_rcp_f32_e32 v32, v32
	v_rcp_f32_e32 v33, v33
	v_add_f32_e32 v70, 1.0, v70
	v_add_f32_e32 v71, 1.0, v71
	v_rcp_f32_e32 v70, v70
	v_rcp_f32_e32 v71, v71
	v_pk_mul_f32 v[74:75], v[168:169], v[50:51] op_sel_hi:[0,1]
	s_waitcnt vmcnt(7)
	v_lshlrev_b32_e32 v72, 16, v58
	v_and_b32_e32 v73, 0xffff0000, v58
	v_pk_mul_f32 v[18:19], v[74:75], v[18:19]
	v_lshlrev_b32_e32 v58, 16, v59
	v_and_b32_e32 v59, 0xffff0000, v59
	v_pk_fma_f32 v[22:23], v[22:23], v[26:27], v[72:73]
	v_lshlrev_b32_e32 v26, 16, v60
	v_and_b32_e32 v27, 0xffff0000, v60
	v_pk_fma_f32 v[24:25], v[24:25], v[28:29], v[58:59]
	v_lshlrev_b32_e32 v28, 16, v61
	v_and_b32_e32 v29, 0xffff0000, v61
	v_pk_fma_f32 v[18:19], v[18:19], v[32:33], v[26:27]
	v_pk_fma_f32 v[28:29], v[20:21], v[70:71], v[28:29]
	v_cvt_pk_bf16_f32 v20, v22, v23
	v_cvt_pk_bf16_f32 v21, v24, v25
	v_cvt_pk_bf16_f32 v22, v18, v19
	s_nop 0
	v_lshlrev_b32_e32 v18, 16, v20
	v_and_b32_e32 v19, 0xffff0000, v20
	v_max_f32_e64 v19, |v19|, |v19|
	v_max_f32_e64 v18, |v18|, |v18|
	v_cvt_pk_bf16_f32 v23, v28, v29
	v_max_f32_e32 v18, v18, v19
	v_lshlrev_b32_e32 v19, 16, v21
	v_and_b32_e32 v24, 0xffff0000, v21
	v_lshlrev_b32_e32 v26, 16, v23
	v_and_b32_e32 v27, 0xffff0000, v23
	v_max_f32_e64 v24, |v24|, |v24|
	v_max_f32_e64 v19, |v19|, |v19|
	v_max_f32_e64 v27, |v27|, |v27|
	v_max_f32_e64 v26, |v26|, |v26|
	v_max_f32_e32 v19, v19, v24
	v_lshlrev_b32_e32 v24, 16, v22
	v_and_b32_e32 v25, 0xffff0000, v22
	v_max_f32_e32 v26, v26, v27
	v_max3_f32 v24, |v24|, |v25|, v26
	v_max3_f32 v18, v18, v19, v24
	v_max3_f32 v18, v76, 0, v18
	ds_bpermute_b32 v19, v165, v18
	global_store_dwordx4 v[30:31], v[20:23], off offset:256
	s_waitcnt lgkmcnt(0)
	v_max_f32_e32 v19, v19, v19
	v_max_f32_e32 v18, v18, v19
	ds_bpermute_b32 v19, v169, v18
	s_and_saveexec_b64 s[34:35], s[6:7]
	s_cbranch_execz .LBB0_1044
	s_waitcnt lgkmcnt(0)
	v_max_f32_e32 v19, v19, v19
	v_max_f32_e32 v18, v18, v18
	v_lshl_add_u64 v[20:21], v[98:99], 2, s[16:17]
	v_max_f32_e32 v18, v18, v19
	global_atomic_umax v[20:21], v18, off
